# MoBA prologue: km_l fill with all 8 loads in flight; P10/P11: next unit's bias quads prefetched during the current epilogue
# speedup vs baseline: 1.0252x; 1.0252x over previous
; template <bool MLA>
; __device__ __forceinline__ void attn_unit(char* lds, int h, int qb, const bf16_t* Qp, int ldq, const bf16_t* Kp, int ldk, const bf16_t* KRp, const bf16_t* Vp, int ldv,
;                                           unsigned char* Op, int ldo, const float* KMp, const float* rel_bias) {
;     ...
;         for (int i = tid; i < 16 * 128; i += 512) km_l[i] = KMp[i] + KMp[i + 65536];
;         __syncthreads();
;         { const int row = tid >> 1, half = tid & 1;
;           unsigned mask;
;           if (qb <= 3) mask = (1u << qb) - 1u;
;           else { const bf16_t* qrow = Qp + (size_t)(q0 + row) * ldq + half * 64;
;               u32x4 qv[8];
; #pragma unroll
;               for (int c = 0; c < 8; ++c) qv[c] = *(const u32x4*)(qrow + c * 8);
;               float v0 = NEG, v1 = NEG, v2 = NEG; int i0 = 0, i1 = 0, i2 = 0;
.LBB0_1535:
	v_add_co_u32_e32 v8, vcc, 0x40000, v4
	s_mov_b64 s[98:99], 0x1000
	s_nop 0
	v_addc_co_u32_e32 v9, vcc, 0, v5, vcc
	v_lshl_add_u64 v[232:233], v[4:5], 0, s[98:99]
	v_lshl_add_u64 v[234:235], v[8:9], 0, s[98:99]
	global_load_dword v236, v[4:5], off
	global_load_dword v237, v[8:9], off
	global_load_dword v238, v[4:5], off offset:2048
	global_load_dword v239, v[8:9], off offset:2048
	global_load_dword v240, v[232:233], off
	global_load_dword v241, v[234:235], off
	global_load_dword v242, v[232:233], off offset:2048
	global_load_dword v243, v[234:235], off offset:2048
	s_waitcnt vmcnt(0)
	v_add_f32_e32 v236, v236, v237
	v_add_f32_e32 v238, v238, v239
	v_add_f32_e32 v240, v240, v241
	v_add_f32_e32 v242, v242, v243
	ds_write_b32 v2, v236
	ds_write_b32 v2, v238 offset:2048
	ds_write_b32 v2, v240 offset:4096
	ds_write_b32 v2, v242 offset:6144
	s_or_b64 exec, exec, s[52:53]
	s_cmp_gt_u32 s26, 3
	s_mov_b64 s[52:53], -1
	s_waitcnt lgkmcnt(0)
	s_barrier
	s_cbranch_scc0 .LBB0_1546
	v_add_u32_e32 v2, s65, v189
	v_mov_b64_e32 v[4:5], s[12:13]
	v_mad_u64_u32 v[4:5], s[12:13], v2, s60, v[4:5]
	v_mov_b32_e32 v177, v3
	v_lshl_add_u64 v[4:5], v[4:5], 0, v[176:177]
	global_load_dwordx4 v[16:19], v[4:5], off offset:2064
	global_load_dwordx4 v[20:23], v[4:5], off offset:2048
	global_load_dwordx4 v[32:35], v[4:5], off offset:2096
	global_load_dwordx4 v[36:39], v[4:5], off offset:2080
	global_load_dwordx4 v[48:51], v[4:5], off offset:2128
	global_load_dwordx4 v[52:55], v[4:5], off offset:2112
	global_load_dwordx4 v[64:67], v[4:5], off offset:2160
	global_load_dwordx4 v[70:73], v[4:5], off offset:2144
	v_and_b32_e32 v4, 64, v195
	v_xor_b32_e32 v2, 1, v195
	v_add_u32_e32 v4, 64, v4
	v_cmp_lt_i32_e32 vcc, v2, v4
	v_mov_b32_e32 v69, 0
	s_mov_b32 s67, 0
	v_cndmask_b32_e32 v2, v195, v2, vcc
	v_lshlrev_b32_e32 v2, 2, v2
	v_mov_b32_e32 v75, 0xff800000
	v_mov_b32_e32 v74, 0
	s_waitcnt vmcnt(7)
	v_lshlrev_b32_e32 v5, 16, v16
	s_waitcnt vmcnt(6)
	v_lshlrev_b32_e32 v4, 16, v20
	v_and_b32_e32 v7, 0xffff0000, v16
	v_and_b32_e32 v6, 0xffff0000, v20
	v_lshlrev_b32_e32 v9, 16, v17
	v_lshlrev_b32_e32 v8, 16, v21
	v_and_b32_e32 v11, 0xffff0000, v17
	v_and_b32_e32 v10, 0xffff0000, v21
	v_lshlrev_b32_e32 v13, 16, v18
	v_lshlrev_b32_e32 v12, 16, v22
	v_and_b32_e32 v15, 0xffff0000, v18
	v_and_b32_e32 v14, 0xffff0000, v22
	v_lshlrev_b32_e32 v17, 16, v19
	v_lshlrev_b32_e32 v16, 16, v23
	v_and_b32_e32 v19, 0xffff0000, v19
	v_and_b32_e32 v18, 0xffff0000, v23
	s_waitcnt vmcnt(5)
	v_lshlrev_b32_e32 v21, 16, v32
	s_waitcnt vmcnt(4)
	v_lshlrev_b32_e32 v20, 16, v36
	v_and_b32_e32 v23, 0xffff0000, v32
	v_and_b32_e32 v22, 0xffff0000, v36
	v_lshlrev_b32_e32 v25, 16, v33
	v_lshlrev_b32_e32 v24, 16, v37
	v_and_b32_e32 v27, 0xffff0000, v33
	v_and_b32_e32 v26, 0xffff0000, v37
	v_lshlrev_b32_e32 v29, 16, v34
	v_lshlrev_b32_e32 v28, 16, v38
	v_and_b32_e32 v31, 0xffff0000, v34
	v_and_b32_e32 v30, 0xffff0000, v38
	v_lshlrev_b32_e32 v33, 16, v35
	v_lshlrev_b32_e32 v32, 16, v39
	v_and_b32_e32 v35, 0xffff0000, v35
	v_and_b32_e32 v34, 0xffff0000, v39
	s_waitcnt vmcnt(3)
	v_lshlrev_b32_e32 v37, 16, v48
	s_waitcnt vmcnt(2)
	v_lshlrev_b32_e32 v36, 16, v52
	v_and_b32_e32 v39, 0xffff0000, v48
	v_and_b32_e32 v38, 0xffff0000, v52
	v_lshlrev_b32_e32 v41, 16, v49
	v_lshlrev_b32_e32 v40, 16, v53
	v_and_b32_e32 v43, 0xffff0000, v49
	v_and_b32_e32 v42, 0xffff0000, v53
	v_lshlrev_b32_e32 v45, 16, v50
	v_lshlrev_b32_e32 v44, 16, v54
	v_and_b32_e32 v47, 0xffff0000, v50
	v_and_b32_e32 v46, 0xffff0000, v54
	v_lshlrev_b32_e32 v49, 16, v51
	v_lshlrev_b32_e32 v48, 16, v55
	v_and_b32_e32 v51, 0xffff0000, v51
	v_and_b32_e32 v50, 0xffff0000, v55
	s_waitcnt vmcnt(1)
	v_lshlrev_b32_e32 v53, 16, v64
	s_waitcnt vmcnt(0)
	v_lshlrev_b32_e32 v52, 16, v70
	v_and_b32_e32 v55, 0xffff0000, v64
	v_and_b32_e32 v54, 0xffff0000, v70
	v_lshlrev_b32_e32 v57, 16, v65
	v_lshlrev_b32_e32 v56, 16, v71
	v_and_b32_e32 v59, 0xffff0000, v65
	v_and_b32_e32 v58, 0xffff0000, v71
	v_lshlrev_b32_e32 v61, 16, v66
	v_lshlrev_b32_e32 v60, 16, v72
	v_and_b32_e32 v63, 0xffff0000, v66
	v_and_b32_e32 v62, 0xffff0000, v72
	v_lshlrev_b32_e32 v65, 16, v67
	v_lshlrev_b32_e32 v64, 16, v73
	v_and_b32_e32 v67, 0xffff0000, v67
	v_and_b32_e32 v66, 0xffff0000, v73
	v_mov_b32_e32 v71, 0xff800000
	v_mov_b32_e32 v70, v167
	v_mov_b32_e32 v72, 0xff800000
	v_mov_b32_e32 v73, 0

;     __device__ bool next(int i, Unit& u) const {
;         const int L = i * G + c; if (L >= ntiles * nN) return false;
;         const int ti = L / nN, pn = L % nN;
;         const int e = __builtin_amdgcn_readfirstlane(tile_e[ti]);
;         u.row0 = ti * BM; u.col0 = pn * BM; u.e = e; u.A = A + (size_t)ti * atile; u.B = B + (size_t)e * bexp + (size_t)pn * btile; return true;
; template <class Epi, class Sched, bool F8 = false, bool MID = false, bool GATHER = false>
; __device__ __forceinline__ void gemm_phase(LAS unsigned char* lds, const Gemm g, const Sched& S, const Epi& E) {
;     ...
;     if constexpr (GATHER) { Unit uu;
;         for (int i = 0; i < 20 && S.next(i, uu); ++i) if (tid < 256) { const int l_ = uu.row0 - g.tab[uu.e] + tid; rt[i * 256 + tid] = l_ < g.tab[32 + uu.e] ? g.list[uu.e * T + l_] : T; }
;         asm volatile("s_waitcnt vmcnt(0) lgkmcnt(0)" ::: "memory"); __builtin_amdgcn_s_barrier(); asm volatile("" ::: "memory");
.LBB0_2358:
	s_mov_b32 s101, 0
	s_load_dwordx2 s[50:51], s[0:1], 0x80
	s_load_dwordx2 s[52:53], s[0:1], 0x90
	s_mov_b32 s13, 0x20000
	v_mbcnt_lo_u32_b32 v1, -1, 0
	v_mbcnt_hi_u32_b32 v1, -1, v1
	v_mul_lo_u32 v2, v1, s82
	v_add_u32_e32 v2, s2, v2
	v_cmp_gt_i32_e32 vcc, s39, v2
	v_lshrrev_b32_e32 v3, 4, v2
	v_min_u32_e32 v4, 0x13f, v3
	v_lshlrev_b32_e32 v4, 2, v4
	v_add_u32_e32 v4, 0x25a04, v4
	ds_read_b32 v5, v4
	s_mov_b64 s[54:55], vcc
	s_waitcnt lgkmcnt(0)
	v_lshlrev_b32_e32 v6, 2, v5
	v_add_u32_e32 v6, 0x25800, v6
	ds_read2_b32 v[6:7], v6 offset1:32
	v_lshlrev_b32_e32 v3, 8, v3
	v_cmp_gt_u32_e32 vcc, 0x100, v0
	v_lshl_add_u32 v1, v0, 2, s13
	s_mov_b64 s[56:57], vcc
	s_waitcnt lgkmcnt(0)
	v_sub_u32_e32 v3, v3, v6
	s_bitcmp1_b32 s54, 0
	s_cbranch_scc0 .Lrt_issued
	v_readlane_b32 s4, v5, 0
	v_readlane_b32 s5, v3, 0
	v_readlane_b32 s22, v7, 0
	v_mov_b32_e32 v200, 0x4000
	s_nop 1
	v_add_u32_e32 v8, s5, v0
	v_cmp_gt_i32_e32 vcc, s22, v8
	s_lshl_b32 s4, s4, 14
	s_nop 0
	s_and_b64 vcc, vcc, s[56:57]
	v_add_lshl_u32 v8, v8, s4, 2
	s_and_saveexec_b64 s[26:27], vcc
	global_load_dword v200, v8, s[48:49]
	s_mov_b64 exec, s[26:27]
	s_bitcmp1_b32 s54, 1
	s_cbranch_scc0 .Lrt_issued
	v_readlane_b32 s4, v5, 1
	v_readlane_b32 s5, v3, 1
	v_readlane_b32 s22, v7, 1
	v_mov_b32_e32 v201, 0x4000
	s_nop 1
	v_add_u32_e32 v8, s5, v0
	v_cmp_gt_i32_e32 vcc, s22, v8
	s_lshl_b32 s4, s4, 14
	s_nop 0
	s_and_b64 vcc, vcc, s[56:57]
	v_add_lshl_u32 v8, v8, s4, 2
	s_and_saveexec_b64 s[26:27], vcc
	global_load_dword v201, v8, s[48:49]
	s_mov_b64 exec, s[26:27]
	s_bitcmp1_b32 s54, 2
	s_cbranch_scc0 .Lrt_issued
	v_readlane_b32 s4, v5, 2
	v_readlane_b32 s5, v3, 2
	v_readlane_b32 s22, v7, 2
	v_mov_b32_e32 v202, 0x4000
	s_nop 1
	v_add_u32_e32 v8, s5, v0
	v_cmp_gt_i32_e32 vcc, s22, v8
	s_lshl_b32 s4, s4, 14
	s_nop 0
	s_and_b64 vcc, vcc, s[56:57]
	v_add_lshl_u32 v8, v8, s4, 2
	s_and_saveexec_b64 s[26:27], vcc
	global_load_dword v202, v8, s[48:49]
	s_mov_b64 exec, s[26:27]
	s_bitcmp1_b32 s54, 3
	s_cbranch_scc0 .Lrt_issued
	v_readlane_b32 s4, v5, 3
	v_readlane_b32 s5, v3, 3
	v_readlane_b32 s22, v7, 3
	v_mov_b32_e32 v203, 0x4000
	s_nop 1
	v_add_u32_e32 v8, s5, v0
	v_cmp_gt_i32_e32 vcc, s22, v8
	s_lshl_b32 s4, s4, 14
	s_nop 0
	s_and_b64 vcc, vcc, s[56:57]
	v_add_lshl_u32 v8, v8, s4, 2
	s_and_saveexec_b64 s[26:27], vcc
	global_load_dword v203, v8, s[48:49]
	s_mov_b64 exec, s[26:27]
	s_bitcmp1_b32 s54, 4
	s_cbranch_scc0 .Lrt_issued
	v_readlane_b32 s4, v5, 4
	v_readlane_b32 s5, v3, 4
	v_readlane_b32 s22, v7, 4
	v_mov_b32_e32 v204, 0x4000
	s_nop 1
	v_add_u32_e32 v8, s5, v0
	v_cmp_gt_i32_e32 vcc, s22, v8
	s_lshl_b32 s4, s4, 14
	s_nop 0
	s_and_b64 vcc, vcc, s[56:57]
	v_add_lshl_u32 v8, v8, s4, 2
	s_and_saveexec_b64 s[26:27], vcc
	global_load_dword v204, v8, s[48:49]
	s_mov_b64 exec, s[26:27]
	s_bitcmp1_b32 s54, 5
	s_cbranch_scc0 .Lrt_issued
	v_readlane_b32 s4, v5, 5
	v_readlane_b32 s5, v3, 5
	v_readlane_b32 s22, v7, 5
	v_mov_b32_e32 v205, 0x4000
	s_nop 1
	v_add_u32_e32 v8, s5, v0
	v_cmp_gt_i32_e32 vcc, s22, v8
	s_lshl_b32 s4, s4, 14
	s_nop 0
	s_and_b64 vcc, vcc, s[56:57]
	v_add_lshl_u32 v8, v8, s4, 2
	s_and_saveexec_b64 s[26:27], vcc
	global_load_dword v205, v8, s[48:49]
	s_mov_b64 exec, s[26:27]
	s_bitcmp1_b32 s54, 6
	s_cbranch_scc0 .Lrt_issued
	v_readlane_b32 s4, v5, 6
	v_readlane_b32 s5, v3, 6
	v_readlane_b32 s22, v7, 6
	v_mov_b32_e32 v206, 0x4000
	s_nop 1
	v_add_u32_e32 v8, s5, v0
	v_cmp_gt_i32_e32 vcc, s22, v8
	s_lshl_b32 s4, s4, 14
	s_nop 0
	s_and_b64 vcc, vcc, s[56:57]
	v_add_lshl_u32 v8, v8, s4, 2
	s_and_saveexec_b64 s[26:27], vcc
	global_load_dword v206, v8, s[48:49]
	s_mov_b64 exec, s[26:27]
	s_bitcmp1_b32 s54, 7
	s_cbranch_scc0 .Lrt_issued
	v_readlane_b32 s4, v5, 7
	v_readlane_b32 s5, v3, 7
	v_readlane_b32 s22, v7, 7
	v_mov_b32_e32 v207, 0x4000
	s_nop 1
	v_add_u32_e32 v8, s5, v0
	v_cmp_gt_i32_e32 vcc, s22, v8
	s_lshl_b32 s4, s4, 14
	s_nop 0
	s_and_b64 vcc, vcc, s[56:57]
	v_add_lshl_u32 v8, v8, s4, 2
	s_and_saveexec_b64 s[26:27], vcc
	global_load_dword v207, v8, s[48:49]
	s_mov_b64 exec, s[26:27]
	s_bitcmp1_b32 s54, 8
	s_cbranch_scc0 .Lrt_issued
	v_readlane_b32 s4, v5, 8
	v_readlane_b32 s5, v3, 8
	v_readlane_b32 s22, v7, 8
	v_mov_b32_e32 v208, 0x4000
	s_nop 1
	v_add_u32_e32 v8, s5, v0
	v_cmp_gt_i32_e32 vcc, s22, v8
	s_lshl_b32 s4, s4, 14
	s_nop 0
	s_and_b64 vcc, vcc, s[56:57]
	v_add_lshl_u32 v8, v8, s4, 2
	s_and_saveexec_b64 s[26:27], vcc
	global_load_dword v208, v8, s[48:49]
	s_mov_b64 exec, s[26:27]
	s_bitcmp1_b32 s54, 9
	s_cbranch_scc0 .Lrt_issued
; template <class Epi, class Sched, bool F8 = false, bool MID = false, bool GATHER = false>
; __device__ __forceinline__ void gemm_phase(LAS unsigned char* lds, const Gemm g, const Sched& S, const Epi& E) {
;     ...
;     if constexpr (GATHER) { Unit uu;
;         for (int i = 0; i < 20 && S.next(i, uu); ++i) if (tid < 256) { const int l_ = uu.row0 - g.tab[uu.e] + tid; rt[i * 256 + tid] = l_ < g.tab[32 + uu.e] ? g.list[uu.e * T + l_] : T; }
;         asm volatile("s_waitcnt vmcnt(0) lgkmcnt(0)" ::: "memory"); __builtin_amdgcn_s_barrier(); asm volatile("" ::: "memory");
	v_readlane_b32 s4, v5, 9
	v_readlane_b32 s5, v3, 9
	v_readlane_b32 s22, v7, 9
	v_mov_b32_e32 v209, 0x4000
	s_nop 1
	v_add_u32_e32 v8, s5, v0
	v_cmp_gt_i32_e32 vcc, s22, v8
	s_lshl_b32 s4, s4, 14
	s_nop 0
	s_and_b64 vcc, vcc, s[56:57]
	v_add_lshl_u32 v8, v8, s4, 2
	s_and_saveexec_b64 s[26:27], vcc
	global_load_dword v209, v8, s[48:49]
	s_mov_b64 exec, s[26:27]
	s_bitcmp1_b32 s54, 10
	s_cbranch_scc0 .Lrt_issued
	v_readlane_b32 s4, v5, 10
	v_readlane_b32 s5, v3, 10
	v_readlane_b32 s22, v7, 10
	v_mov_b32_e32 v210, 0x4000
	s_nop 1
	v_add_u32_e32 v8, s5, v0
	v_cmp_gt_i32_e32 vcc, s22, v8
	s_lshl_b32 s4, s4, 14
	s_nop 0
	s_and_b64 vcc, vcc, s[56:57]
	v_add_lshl_u32 v8, v8, s4, 2
	s_and_saveexec_b64 s[26:27], vcc
	global_load_dword v210, v8, s[48:49]
	s_mov_b64 exec, s[26:27]
	s_bitcmp1_b32 s54, 11
	s_cbranch_scc0 .Lrt_issued
	v_readlane_b32 s4, v5, 11
	v_readlane_b32 s5, v3, 11
	v_readlane_b32 s22, v7, 11
	v_mov_b32_e32 v211, 0x4000
	s_nop 1
	v_add_u32_e32 v8, s5, v0
	v_cmp_gt_i32_e32 vcc, s22, v8
	s_lshl_b32 s4, s4, 14
	s_nop 0
	s_and_b64 vcc, vcc, s[56:57]
	v_add_lshl_u32 v8, v8, s4, 2
	s_and_saveexec_b64 s[26:27], vcc
	global_load_dword v211, v8, s[48:49]
	s_mov_b64 exec, s[26:27]
	s_bitcmp1_b32 s54, 12
	s_cbranch_scc0 .Lrt_issued
	v_readlane_b32 s4, v5, 12
	v_readlane_b32 s5, v3, 12
	v_readlane_b32 s22, v7, 12
	v_mov_b32_e32 v212, 0x4000
	s_nop 1
	v_add_u32_e32 v8, s5, v0
	v_cmp_gt_i32_e32 vcc, s22, v8
	s_lshl_b32 s4, s4, 14
	s_nop 0
	s_and_b64 vcc, vcc, s[56:57]
	v_add_lshl_u32 v8, v8, s4, 2
	s_and_saveexec_b64 s[26:27], vcc
	global_load_dword v212, v8, s[48:49]
	s_mov_b64 exec, s[26:27]
	s_bitcmp1_b32 s54, 13
	s_cbranch_scc0 .Lrt_issued
	v_readlane_b32 s4, v5, 13
	v_readlane_b32 s5, v3, 13
	v_readlane_b32 s22, v7, 13
	v_mov_b32_e32 v213, 0x4000
	s_nop 1
	v_add_u32_e32 v8, s5, v0
	v_cmp_gt_i32_e32 vcc, s22, v8
	s_lshl_b32 s4, s4, 14
	s_nop 0
	s_and_b64 vcc, vcc, s[56:57]
	v_add_lshl_u32 v8, v8, s4, 2
	s_and_saveexec_b64 s[26:27], vcc
	global_load_dword v213, v8, s[48:49]
	s_mov_b64 exec, s[26:27]
	s_bitcmp1_b32 s54, 14
	s_cbranch_scc0 .Lrt_issued
	v_readlane_b32 s4, v5, 14
	v_readlane_b32 s5, v3, 14
	v_readlane_b32 s22, v7, 14
	v_mov_b32_e32 v214, 0x4000
	s_nop 1
	v_add_u32_e32 v8, s5, v0
	v_cmp_gt_i32_e32 vcc, s22, v8
	s_lshl_b32 s4, s4, 14
	s_nop 0
	s_and_b64 vcc, vcc, s[56:57]
	v_add_lshl_u32 v8, v8, s4, 2
	s_and_saveexec_b64 s[26:27], vcc
	global_load_dword v214, v8, s[48:49]
	s_mov_b64 exec, s[26:27]
	s_bitcmp1_b32 s54, 15
	s_cbranch_scc0 .Lrt_issued
	v_readlane_b32 s4, v5, 15
	v_readlane_b32 s5, v3, 15
	v_readlane_b32 s22, v7, 15
	v_mov_b32_e32 v215, 0x4000
	s_nop 1
	v_add_u32_e32 v8, s5, v0
	v_cmp_gt_i32_e32 vcc, s22, v8
	s_lshl_b32 s4, s4, 14
	s_nop 0
	s_and_b64 vcc, vcc, s[56:57]
	v_add_lshl_u32 v8, v8, s4, 2
	s_and_saveexec_b64 s[26:27], vcc
	global_load_dword v215, v8, s[48:49]
	s_mov_b64 exec, s[26:27]
	s_bitcmp1_b32 s54, 16
	s_cbranch_scc0 .Lrt_issued
	v_readlane_b32 s4, v5, 16
	v_readlane_b32 s5, v3, 16
	v_readlane_b32 s22, v7, 16
	v_mov_b32_e32 v216, 0x4000
	s_nop 1
	v_add_u32_e32 v8, s5, v0
	v_cmp_gt_i32_e32 vcc, s22, v8
	s_lshl_b32 s4, s4, 14
	s_nop 0
	s_and_b64 vcc, vcc, s[56:57]
	v_add_lshl_u32 v8, v8, s4, 2
	s_and_saveexec_b64 s[26:27], vcc
	global_load_dword v216, v8, s[48:49]
	s_mov_b64 exec, s[26:27]
	s_bitcmp1_b32 s54, 17
	s_cbranch_scc0 .Lrt_issued
	v_readlane_b32 s4, v5, 17
	v_readlane_b32 s5, v3, 17
	v_readlane_b32 s22, v7, 17
	v_mov_b32_e32 v217, 0x4000
	s_nop 1
	v_add_u32_e32 v8, s5, v0
	v_cmp_gt_i32_e32 vcc, s22, v8
	s_lshl_b32 s4, s4, 14
	s_nop 0
	s_and_b64 vcc, vcc, s[56:57]
	v_add_lshl_u32 v8, v8, s4, 2
	s_and_saveexec_b64 s[26:27], vcc
	global_load_dword v217, v8, s[48:49]
	s_mov_b64 exec, s[26:27]
	s_bitcmp1_b32 s54, 18
	s_cbranch_scc0 .Lrt_issued
	v_readlane_b32 s4, v5, 18
	v_readlane_b32 s5, v3, 18
	v_readlane_b32 s22, v7, 18
	v_mov_b32_e32 v218, 0x4000
	s_nop 1
	v_add_u32_e32 v8, s5, v0
	v_cmp_gt_i32_e32 vcc, s22, v8
	s_lshl_b32 s4, s4, 14
	s_nop 0
	s_and_b64 vcc, vcc, s[56:57]
	v_add_lshl_u32 v8, v8, s4, 2
	s_and_saveexec_b64 s[26:27], vcc
	global_load_dword v218, v8, s[48:49]
	s_mov_b64 exec, s[26:27]
	s_bitcmp1_b32 s54, 19
	s_cbranch_scc0 .Lrt_issued
	v_readlane_b32 s4, v5, 19
	v_readlane_b32 s5, v3, 19
	v_readlane_b32 s22, v7, 19
	v_mov_b32_e32 v219, 0x4000
	s_nop 1
	v_add_u32_e32 v8, s5, v0
	v_cmp_gt_i32_e32 vcc, s22, v8
	s_lshl_b32 s4, s4, 14
	s_nop 0
	s_and_b64 vcc, vcc, s[56:57]
	v_add_lshl_u32 v8, v8, s4, 2
	s_and_saveexec_b64 s[26:27], vcc
	global_load_dword v219, v8, s[48:49]
	s_mov_b64 exec, s[26:27]

; __device__ __forceinline__ unsigned cvt4_fp8(float a, float b, float c, float d) { int w = 0; w = __builtin_amdgcn_cvt_pk_fp8_f32(a, b, w, false); w = __builtin_amdgcn_cvt_pk_fp8_f32(c, d, w, true); return (unsigned)w; }
; __device__ __forceinline__ float sigmoidf_(float x) { return __builtin_amdgcn_rcpf(1.0f + __expf(-x)); }
;     __device__ __forceinline__ void operator()(const Acc& acc, const Unit& u, int wr, int wc, int fr, int fq) const {
;         const int row0 = u.row0 + wr * 64 + fr, hc = (u.col0 >> 1) + wc * 32 + 8 * fq;
;         const float* bgp = bg + (size_t)u.e * DM + hc; const float* bup = bu + (size_t)u.e * DM + hc;
;         const f32x4 bg0 = *(const f32x4*)bgp, bg1 = *(const f32x4*)(bgp + 4), bu0 = *(const f32x4*)bup, bu1 = *(const f32x4*)(bup + 4);
; #pragma unroll
;         for (int ai = 0; ai < 2; ++ai)
; #pragma unroll
;             for (int m = 0; m < 4; ++m) { f32x4 g0 = acc[ai][0][m][0] + bg0, g1 = acc[ai][0][m][1] + bg1, u0 = acc[ai][1][m][0] + bu0, u1 = acc[ai][1][m][1] + bu1, r0, r1;
; #pragma unroll
;                 for (int j = 0; j < 4; ++j) {
;                     const float ga = fminf(g0[j], 7.0f), gb = fminf(g1[j], 7.0f);
;                     const float ua = fminf(fmaxf(u0[j], -7.0f), 7.0f), ub = fminf(fmaxf(u1[j], -7.0f), 7.0f);
;                     r0[j] = ga * sigmoidf_(1.702f * ga) * (ua + 1.0f); r1[j] = gb * sigmoidf_(1.702f * gb) * (ub + 1.0f); }
;                 u32x2 w; w.x = cvt4_fp8(r0[0], r0[1], r0[2], r0[3]); w.y = cvt4_fp8(r1[0], r1[1], r1[2], r1[3]);
;                 *(u32x2*)(O + (size_t)(row0 + ai * HALF + m * 16) * DM + hc) = w; }
.LBB0_2477:
	s_nop 15
	s_nop 15
	v_mbcnt_lo_u32_b32 v20, -1, 0
	v_mbcnt_hi_u32_b32 v20, -1, v20
	s_ashr_i32 s13, s72, 1
	v_ashrrev_i32_e32 v2, 1, v20
	v_and_b32_e32 v2, -8, v2
	s_add_i32 s13, s13, s88
	v_add_u32_e32 v18, s13, v2
	s_ashr_i32 s13, s12, 31
	s_lshl_b64 s[22:23], s[12:13], 13
	s_add_u32 s64, s50, s22
	v_ashrrev_i32_e32 v19, 31, v18
	s_addc_u32 s65, s51, s23
	v_lshlrev_b64 v[6:7], 2, v[18:19]
	v_lshl_add_u64 v[8:9], s[64:65], 0, v[6:7]
	s_cmp_lg_u32 s101, 0
	s_cbranch_scc1 .Lb10_have
	global_load_dwordx4 v[2:5], v[8:9], off offset:16
	global_load_dwordx4 v[14:17], v[8:9], off
	s_add_u32 s22, s52, s22
	s_addc_u32 s23, s53, s23
	v_lshl_add_u64 v[6:7], s[22:23], 0, v[6:7]
	global_load_dwordx4 v[10:13], v[6:7], off
	s_nop 0
	global_load_dwordx4 v[6:9], v[6:7], off offset:16
	s_branch .Lb10_join
.Lb10_have:
	v_mov_b32_e32 v2, v218
	v_mov_b32_e32 v3, v219
	v_mov_b32_e32 v4, v220
	v_mov_b32_e32 v5, v221
	v_mov_b32_e32 v14, v222
	v_mov_b32_e32 v15, v223
	v_mov_b32_e32 v16, v224
	v_mov_b32_e32 v17, v225
	v_mov_b32_e32 v10, v226
	v_mov_b32_e32 v11, v227
	v_mov_b32_e32 v12, v228
	v_mov_b32_e32 v13, v229
	v_mov_b32_e32 v6, v230
	v_mov_b32_e32 v7, v231
	v_mov_b32_e32 v8, v232
	v_mov_b32_e32 v9, v233
.Lb10_join:
	v_and_or_b32 v20, v20, 15, s87
	v_add_u32_e32 v20, s41, v20
	s_mov_b32 s13, 0x8000
	s_waitcnt vmcnt(3)
	v_add_f32_e32 v22, v154, v2
	v_min_f32_e32 v22, 0x40e00000, v22
	v_mul_f32_e32 v185, 0x3fd9db23, v22
	v_mul_f32_e32 v185, 0xbfb8aa3b, v185
	v_exp_f32_e32 v185, v185
	s_waitcnt vmcnt(2)
	v_add_f32_e32 v21, v158, v14
	v_add_f32_e32 v25, v159, v15
	v_add_f32_e32 v26, v155, v3
	v_min_f32_e32 v21, 0x40e00000, v21
	v_min_f32_e32 v25, 0x40e00000, v25
	v_min_f32_e32 v26, 0x40e00000, v26
	v_mul_f32_e32 v184, 0x3fd9db23, v21
	v_mul_f32_e32 v186, 0x3fd9db23, v25
	v_mul_f32_e32 v187, 0x3fd9db23, v26
	v_mul_f32_e32 v184, 0xbfb8aa3b, v184
	v_mul_f32_e32 v186, 0xbfb8aa3b, v186
	v_mul_f32_e32 v187, 0xbfb8aa3b, v187
	v_add_f32_e32 v185, 1.0, v185
	v_exp_f32_e32 v184, v184
	v_exp_f32_e32 v186, v186
	v_exp_f32_e32 v187, v187
	v_rcp_f32_e32 v185, v185
	s_waitcnt vmcnt(0)
	s_mov_b32 s101, 0
	s_and_b64 vcc, exec, s[4:5]
	s_cbranch_vccnz .Lb10_nonext
	s_ashr_i32 s98, s3, 1
	s_add_i32 s98, s98, s88
	s_lshl_b32 s99, s56, 13
	v_mbcnt_lo_u32_b32 v248, -1, 0
	v_mbcnt_hi_u32_b32 v248, -1, v248
	v_ashrrev_i32_e32 v248, 1, v248
	v_and_b32_e32 v248, -8, v248
	v_add_u32_e32 v248, s98, v248
	v_lshl_add_u32 v248, v248, 2, s99
	global_load_dwordx4 v[218:221], v248, s[50:51] offset:16
	global_load_dwordx4 v[222:225], v248, s[50:51]
	global_load_dwordx4 v[226:229], v248, s[52:53]
	global_load_dwordx4 v[230:233], v248, s[52:53] offset:16
	s_mov_b32 s101, 1
.Lb10_nonext:
	v_add_f32_e32 v24, v122, v6
	v_add_f32_e32 v30, v156, v4
	v_add_f32_e32 v33, v161, v17
	v_med3_f32 v24, v24, s97, v176
	v_min_f32_e32 v30, 0x40e00000, v30
	v_min_f32_e32 v33, 0x40e00000, v33
	v_add_f32_e32 v24, 1.0, v24
	v_mul_f32_e32 v189, 0x3fd9db23, v30
	v_add_f32_e32 v184, 1.0, v184
	v_add_f32_e32 v186, 1.0, v186
	v_add_f32_e32 v187, 1.0, v187
	v_mul_f32_e32 v22, v22, v185
	v_mul_f32_e32 v189, 0xbfb8aa3b, v189
	v_rcp_f32_e32 v184, v184
	v_rcp_f32_e32 v186, v186
	v_rcp_f32_e32 v187, v187
	v_mul_f32_e32 v24, v24, v22
	v_mul_f32_e32 v22, 0x3fd9db23, v33
	v_add_f32_e32 v29, v160, v16
	v_exp_f32_e32 v189, v189
	v_mul_f32_e32 v22, 0xbfb8aa3b, v22
	v_add_f32_e32 v23, v126, v10
	v_add_f32_e32 v27, v127, v11
	v_add_f32_e32 v28, v123, v7
	v_min_f32_e32 v29, 0x40e00000, v29
	v_exp_f32_e32 v22, v22
	v_add_f32_e32 v181, v157, v5
	v_med3_f32 v23, v23, s97, v176
	v_med3_f32 v27, v27, s97, v176
	v_med3_f32 v28, v28, s97, v176
	v_mul_f32_e32 v188, 0x3fd9db23, v29
	v_min_f32_e32 v181, 0x40e00000, v181
	v_add_f32_e32 v23, 1.0, v23
	v_add_f32_e32 v27, 1.0, v27
	v_add_f32_e32 v28, 1.0, v28
	v_mul_f32_e32 v188, 0xbfb8aa3b, v188
	v_mul_f32_e32 v21, v21, v184
	v_mul_f32_e32 v25, v25, v186
	v_mul_f32_e32 v26, v26, v187
	v_exp_f32_e32 v188, v188
	v_add_f32_e32 v189, 1.0, v189
	v_mul_f32_e32 v21, v23, v21
	v_mul_f32_e32 v23, v27, v25
	v_mul_f32_e32 v25, v28, v26
	v_mul_f32_e32 v28, 0x3fd9db23, v181
	v_rcp_f32_e32 v189, v189
	v_mul_f32_e32 v28, 0xbfb8aa3b, v28
	v_add_f32_e32 v22, 1.0, v22
	v_exp_f32_e32 v28, v28
	v_rcp_f32_e32 v22, v22
	v_add_f32_e32 v32, v124, v8
	v_add_f32_e32 v182, v129, v13
	v_med3_f32 v32, v32, s97, v176
	v_add_f32_e32 v188, 1.0, v188
	v_med3_f32 v182, v182, s97, v176
	v_add_f32_e32 v32, 1.0, v32
	v_rcp_f32_e32 v188, v188
	v_mul_f32_e32 v30, v30, v189
	v_mul_f32_e32 v27, v32, v30
	v_add_f32_e32 v28, 1.0, v28
	v_mul_f32_e32 v22, v33, v22
	v_add_f32_e32 v30, 1.0, v182
	v_add_f32_e32 v31, v128, v12
	v_rcp_f32_e32 v28, v28
	v_mul_f32_e32 v30, v30, v22
	v_mov_b32_e32 v22, 0
	v_med3_f32 v31, v31, s97, v176
	v_cvt_pk_fp8_f32 v22, v21, v23
	v_mov_b32_e32 v23, 0
	v_add_f32_e32 v183, v125, v9
	v_add_f32_e32 v31, 1.0, v31
	v_mul_f32_e32 v29, v29, v188
	v_cvt_pk_fp8_f32 v23, v24, v25
	v_mul_f32_e32 v26, v31, v29
	v_med3_f32 v29, v183, s97, v176
	v_mul_f32_e32 v28, v181, v28
	v_add_f32_e32 v21, 1.0, v29
	v_mul_f32_e32 v21, v21, v28
	v_cvt_pk_fp8_f32 v23, v27, v21 op_sel:[0,0,1]
	v_ashrrev_i32_e32 v21, 31, v20
	v_lshlrev_b64 v[20:21], 11, v[20:21]
	v_lshl_add_u64 v[20:21], s[30:31], 0, v[20:21]
	v_lshl_add_u64 v[18:19], v[20:21], 0, v[18:19]
	v_add_f32_e32 v20, v150, v14
	v_min_f32_e32 v20, 0x40e00000, v20
	v_add_f32_e32 v21, v146, v2
	v_min_f32_e32 v21, 0x40e00000, v21
	v_mul_f32_e32 v24, 0x3fd9db23, v20
	v_mul_f32_e32 v24, 0xbfb8aa3b, v24
	v_mul_f32_e32 v25, 0x3fd9db23, v21
	v_exp_f32_e32 v24, v24
	v_mul_f32_e32 v25, 0xbfb8aa3b, v25
	v_exp_f32_e32 v25, v25
	v_cvt_pk_fp8_f32 v22, v26, v30 op_sel:[0,0,1]
; __device__ __forceinline__ unsigned cvt4_fp8(float a, float b, float c, float d) { int w = 0; w = __builtin_amdgcn_cvt_pk_fp8_f32(a, b, w, false); w = __builtin_amdgcn_cvt_pk_fp8_f32(c, d, w, true); return (unsigned)w; }
; __device__ __forceinline__ float sigmoidf_(float x) { return __builtin_amdgcn_rcpf(1.0f + __expf(-x)); }
;     __device__ __forceinline__ void operator()(const Acc& acc, const Unit& u, int wr, int wc, int fr, int fq) const {
;     ...
;             for (int m = 0; m < 4; ++m) { f32x4 g0 = acc[ai][0][m][0] + bg0, g1 = acc[ai][0][m][1] + bg1, u0 = acc[ai][1][m][0] + bu0, u1 = acc[ai][1][m][1] + bu1, r0, r1;
; #pragma unroll
;                 for (int j = 0; j < 4; ++j) {
;                     const float ga = fminf(g0[j], 7.0f), gb = fminf(g1[j], 7.0f);
;                     const float ua = fminf(fmaxf(u0[j], -7.0f), 7.0f), ub = fminf(fmaxf(u1[j], -7.0f), 7.0f);
;                     r0[j] = ga * sigmoidf_(1.702f * ga) * (ua + 1.0f); r1[j] = gb * sigmoidf_(1.702f * gb) * (ub + 1.0f); }
;                 u32x2 w; w.x = cvt4_fp8(r0[0], r0[1], r0[2], r0[3]); w.y = cvt4_fp8(r1[0], r1[1], r1[2], r1[3]);
;                 *(u32x2*)(O + (size_t)(row0 + ai * HALF + m * 16) * DM + hc) = w; }
	v_add_f32_e32 v24, 1.0, v24
	v_rcp_f32_e32 v24, v24
	v_add_f32_e32 v25, 1.0, v25
	v_rcp_f32_e32 v25, v25
	global_store_dwordx2 v[18:19], v[22:23], off
	v_add_f32_e32 v22, v118, v10
	v_med3_f32 v22, v22, s97, v176
	v_add_f32_e32 v23, v114, v6
	v_med3_f32 v23, v23, s97, v176
	v_mul_f32_e32 v20, v20, v24
	v_add_f32_e32 v22, 1.0, v22
	v_mul_f32_e32 v22, v22, v20
	v_mul_f32_e32 v20, v21, v25
	v_add_f32_e32 v21, 1.0, v23
	v_mul_f32_e32 v23, v21, v20
	v_add_f32_e32 v20, v151, v15
	v_min_f32_e32 v20, 0x40e00000, v20
	v_add_f32_e32 v21, v147, v3
	v_min_f32_e32 v21, 0x40e00000, v21
	v_mul_f32_e32 v26, 0x3fd9db23, v20
	v_mul_f32_e32 v26, 0xbfb8aa3b, v26
	v_mul_f32_e32 v27, 0x3fd9db23, v21
	v_exp_f32_e32 v26, v26
	v_mul_f32_e32 v27, 0xbfb8aa3b, v27
	v_exp_f32_e32 v27, v27
	v_add_f32_e32 v24, v119, v11
	v_add_f32_e32 v26, 1.0, v26
	v_rcp_f32_e32 v26, v26
	v_add_f32_e32 v27, 1.0, v27
	v_rcp_f32_e32 v27, v27
	v_med3_f32 v24, v24, s97, v176
	v_add_f32_e32 v25, v115, v7
	v_med3_f32 v25, v25, s97, v176
	v_mul_f32_e32 v20, v20, v26
	v_add_f32_e32 v24, 1.0, v24
	v_mul_f32_e32 v24, v24, v20
	v_mul_f32_e32 v20, v21, v27
	v_add_f32_e32 v21, 1.0, v25
	v_mul_f32_e32 v25, v21, v20
	v_add_f32_e32 v20, v152, v16
	v_min_f32_e32 v20, 0x40e00000, v20
	v_add_f32_e32 v21, v148, v4
	v_min_f32_e32 v21, 0x40e00000, v21
	v_mul_f32_e32 v28, 0x3fd9db23, v20
	v_mul_f32_e32 v28, 0xbfb8aa3b, v28
	v_mul_f32_e32 v29, 0x3fd9db23, v21
	v_exp_f32_e32 v28, v28
	v_mul_f32_e32 v29, 0xbfb8aa3b, v29
	v_exp_f32_e32 v29, v29
	v_add_f32_e32 v26, v120, v12
	v_add_f32_e32 v28, 1.0, v28
	v_rcp_f32_e32 v28, v28
	v_add_f32_e32 v29, 1.0, v29
	v_rcp_f32_e32 v29, v29
	v_med3_f32 v26, v26, s97, v176
	v_add_f32_e32 v27, v116, v8
	v_med3_f32 v27, v27, s97, v176
	v_mul_f32_e32 v20, v20, v28
	v_add_f32_e32 v26, 1.0, v26
	v_mul_f32_e32 v26, v26, v20
	v_mul_f32_e32 v20, v21, v29
	v_add_f32_e32 v21, 1.0, v27
	v_mul_f32_e32 v27, v21, v20
	v_add_f32_e32 v20, v153, v17
	v_min_f32_e32 v20, 0x40e00000, v20
	v_add_f32_e32 v21, v149, v5
	v_min_f32_e32 v21, 0x40e00000, v21
	v_mul_f32_e32 v30, 0x3fd9db23, v20
	v_mul_f32_e32 v30, 0xbfb8aa3b, v30
	v_mul_f32_e32 v31, 0x3fd9db23, v21
	v_exp_f32_e32 v30, v30
	v_mul_f32_e32 v31, 0xbfb8aa3b, v31
	v_exp_f32_e32 v31, v31
	v_add_f32_e32 v28, v121, v13
	v_add_f32_e32 v30, 1.0, v30
	v_rcp_f32_e32 v30, v30
	v_add_f32_e32 v31, 1.0, v31
	v_rcp_f32_e32 v31, v31
	v_med3_f32 v28, v28, s97, v176
	v_mul_f32_e32 v20, v20, v30
	v_add_f32_e32 v28, 1.0, v28
	v_mul_f32_e32 v28, v28, v20
	v_mul_f32_e32 v30, v21, v31
	v_mov_b32_e32 v20, 0
	v_mov_b32_e32 v21, 0
	v_add_f32_e32 v29, v117, v9
	v_cvt_pk_fp8_f32 v20, v22, v24
	v_cvt_pk_fp8_f32 v21, v23, v25
	v_med3_f32 v29, v29, s97, v176
	v_add_f32_e32 v22, 1.0, v29
	v_mul_f32_e32 v22, v22, v30
	v_cvt_pk_fp8_f32 v20, v26, v28 op_sel:[0,0,1]
	v_cvt_pk_fp8_f32 v21, v27, v22 op_sel:[0,0,1]
	v_add_co_u32_e32 v22, vcc, s13, v18
	s_mov_b32 s13, 0x10000
	s_nop 0
	v_addc_co_u32_e32 v23, vcc, 0, v19, vcc
	global_store_dwordx2 v[22:23], v[20:21], off
	v_add_f32_e32 v20, v142, v14
	v_min_f32_e32 v20, 0x40e00000, v20
	v_add_f32_e32 v21, v138, v2
	v_min_f32_e32 v21, 0x40e00000, v21
	v_mul_f32_e32 v24, 0x3fd9db23, v20
	v_mul_f32_e32 v24, 0xbfb8aa3b, v24
	v_mul_f32_e32 v25, 0x3fd9db23, v21
	v_exp_f32_e32 v24, v24
	v_mul_f32_e32 v25, 0xbfb8aa3b, v25
	v_exp_f32_e32 v25, v25
	v_add_f32_e32 v22, v110, v10
	v_add_f32_e32 v24, 1.0, v24
	v_rcp_f32_e32 v24, v24
	v_add_f32_e32 v25, 1.0, v25
	v_rcp_f32_e32 v25, v25
	v_med3_f32 v22, v22, s97, v176
	v_add_f32_e32 v23, v106, v6
	v_med3_f32 v23, v23, s97, v176
	v_mul_f32_e32 v20, v20, v24
	v_add_f32_e32 v22, 1.0, v22
	v_mul_f32_e32 v22, v22, v20
	v_mul_f32_e32 v20, v21, v25
	v_add_f32_e32 v21, 1.0, v23
	v_mul_f32_e32 v23, v21, v20
	v_add_f32_e32 v20, v143, v15
	v_min_f32_e32 v20, 0x40e00000, v20
	v_add_f32_e32 v21, v139, v3
	v_min_f32_e32 v21, 0x40e00000, v21
	v_mul_f32_e32 v26, 0x3fd9db23, v20
	v_mul_f32_e32 v26, 0xbfb8aa3b, v26
	v_mul_f32_e32 v27, 0x3fd9db23, v21
	v_exp_f32_e32 v26, v26
	v_mul_f32_e32 v27, 0xbfb8aa3b, v27
	v_exp_f32_e32 v27, v27
	v_add_f32_e32 v24, v111, v11
	v_add_f32_e32 v26, 1.0, v26
	v_rcp_f32_e32 v26, v26
	v_add_f32_e32 v27, 1.0, v27
	v_rcp_f32_e32 v27, v27
	v_med3_f32 v24, v24, s97, v176
	v_add_f32_e32 v25, v107, v7
	v_med3_f32 v25, v25, s97, v176
	v_mul_f32_e32 v20, v20, v26
	v_add_f32_e32 v24, 1.0, v24
	v_mul_f32_e32 v24, v24, v20
	v_mul_f32_e32 v20, v21, v27
	v_add_f32_e32 v21, 1.0, v25
	v_mul_f32_e32 v25, v21, v20
	v_add_f32_e32 v20, v144, v16
	v_min_f32_e32 v20, 0x40e00000, v20
	v_add_f32_e32 v21, v140, v4
	v_min_f32_e32 v21, 0x40e00000, v21
	v_mul_f32_e32 v28, 0x3fd9db23, v20
	v_mul_f32_e32 v28, 0xbfb8aa3b, v28
	v_mul_f32_e32 v29, 0x3fd9db23, v21
	v_exp_f32_e32 v28, v28
	v_mul_f32_e32 v29, 0xbfb8aa3b, v29
	v_exp_f32_e32 v29, v29
	v_add_f32_e32 v26, v112, v12
	v_add_f32_e32 v28, 1.0, v28
	v_rcp_f32_e32 v28, v28
	v_add_f32_e32 v29, 1.0, v29
	v_rcp_f32_e32 v29, v29
	v_med3_f32 v26, v26, s97, v176
	v_add_f32_e32 v27, v108, v8
	v_med3_f32 v27, v27, s97, v176
	v_mul_f32_e32 v20, v20, v28
	v_add_f32_e32 v26, 1.0, v26
	v_mul_f32_e32 v26, v26, v20
	v_mul_f32_e32 v20, v21, v29
	v_add_f32_e32 v21, 1.0, v27
	v_mul_f32_e32 v27, v21, v20
	v_add_f32_e32 v20, v145, v17
	v_min_f32_e32 v20, 0x40e00000, v20
	v_add_f32_e32 v21, v141, v5
	v_min_f32_e32 v21, 0x40e00000, v21
	v_mul_f32_e32 v30, 0x3fd9db23, v20
	v_mul_f32_e32 v30, 0xbfb8aa3b, v30
	v_mul_f32_e32 v31, 0x3fd9db23, v21
	v_exp_f32_e32 v30, v30
	v_mul_f32_e32 v31, 0xbfb8aa3b, v31
	v_exp_f32_e32 v31, v31
	v_add_f32_e32 v28, v113, v13
	v_add_f32_e32 v30, 1.0, v30
	v_rcp_f32_e32 v30, v30
	v_add_f32_e32 v31, 1.0, v31
	v_rcp_f32_e32 v31, v31
	v_med3_f32 v28, v28, s97, v176
; __device__ __forceinline__ unsigned cvt4_fp8(float a, float b, float c, float d) { int w = 0; w = __builtin_amdgcn_cvt_pk_fp8_f32(a, b, w, false); w = __builtin_amdgcn_cvt_pk_fp8_f32(c, d, w, true); return (unsigned)w; }
; __device__ __forceinline__ float sigmoidf_(float x) { return __builtin_amdgcn_rcpf(1.0f + __expf(-x)); }
;     __device__ __forceinline__ void operator()(const Acc& acc, const Unit& u, int wr, int wc, int fr, int fq) const {
;     ...
;             for (int m = 0; m < 4; ++m) { f32x4 g0 = acc[ai][0][m][0] + bg0, g1 = acc[ai][0][m][1] + bg1, u0 = acc[ai][1][m][0] + bu0, u1 = acc[ai][1][m][1] + bu1, r0, r1;
; #pragma unroll
;                 for (int j = 0; j < 4; ++j) {
;                     const float ga = fminf(g0[j], 7.0f), gb = fminf(g1[j], 7.0f);
;                     const float ua = fminf(fmaxf(u0[j], -7.0f), 7.0f), ub = fminf(fmaxf(u1[j], -7.0f), 7.0f);
;                     r0[j] = ga * sigmoidf_(1.702f * ga) * (ua + 1.0f); r1[j] = gb * sigmoidf_(1.702f * gb) * (ub + 1.0f); }
;                 u32x2 w; w.x = cvt4_fp8(r0[0], r0[1], r0[2], r0[3]); w.y = cvt4_fp8(r1[0], r1[1], r1[2], r1[3]);
;                 *(u32x2*)(O + (size_t)(row0 + ai * HALF + m * 16) * DM + hc) = w; }
	v_mul_f32_e32 v20, v20, v30
	v_add_f32_e32 v28, 1.0, v28
	v_mul_f32_e32 v28, v28, v20
	v_mul_f32_e32 v30, v21, v31
	v_mov_b32_e32 v20, 0
	v_mov_b32_e32 v21, 0
	v_add_f32_e32 v29, v109, v9
	v_cvt_pk_fp8_f32 v20, v22, v24
	v_cvt_pk_fp8_f32 v21, v23, v25
	v_med3_f32 v29, v29, s97, v176
	v_add_f32_e32 v22, 1.0, v29
	v_mul_f32_e32 v22, v22, v30
	v_cvt_pk_fp8_f32 v20, v26, v28 op_sel:[0,0,1]
	v_cvt_pk_fp8_f32 v21, v27, v22 op_sel:[0,0,1]
	v_add_co_u32_e32 v22, vcc, s13, v18
	s_mov_b32 s13, 0x18000
	s_nop 0
	v_addc_co_u32_e32 v23, vcc, 0, v19, vcc
	global_store_dwordx2 v[22:23], v[20:21], off
	v_add_f32_e32 v20, v134, v14
	v_min_f32_e32 v20, 0x40e00000, v20
	v_add_f32_e32 v21, v130, v2
	v_min_f32_e32 v21, 0x40e00000, v21
	v_mul_f32_e32 v24, 0x3fd9db23, v20
	v_mul_f32_e32 v24, 0xbfb8aa3b, v24
	v_mul_f32_e32 v25, 0x3fd9db23, v21
	v_exp_f32_e32 v24, v24
	v_mul_f32_e32 v25, 0xbfb8aa3b, v25
	v_exp_f32_e32 v25, v25
	v_add_f32_e32 v22, v102, v10
	v_add_f32_e32 v24, 1.0, v24
	v_rcp_f32_e32 v24, v24
	v_add_f32_e32 v25, 1.0, v25
	v_rcp_f32_e32 v25, v25
	v_med3_f32 v22, v22, s97, v176
	v_add_f32_e32 v23, v98, v6
	v_med3_f32 v23, v23, s97, v176
	v_mul_f32_e32 v20, v20, v24
	v_add_f32_e32 v22, 1.0, v22
	v_mul_f32_e32 v22, v22, v20
	v_mul_f32_e32 v20, v21, v25
	v_add_f32_e32 v21, 1.0, v23
	v_mul_f32_e32 v23, v21, v20
	v_add_f32_e32 v20, v135, v15
	v_min_f32_e32 v20, 0x40e00000, v20
	v_add_f32_e32 v21, v131, v3
	v_min_f32_e32 v21, 0x40e00000, v21
	v_mul_f32_e32 v26, 0x3fd9db23, v20
	v_mul_f32_e32 v26, 0xbfb8aa3b, v26
	v_mul_f32_e32 v27, 0x3fd9db23, v21
	v_exp_f32_e32 v26, v26
	v_mul_f32_e32 v27, 0xbfb8aa3b, v27
	v_exp_f32_e32 v27, v27
	v_add_f32_e32 v24, v103, v11
	v_add_f32_e32 v26, 1.0, v26
	v_rcp_f32_e32 v26, v26
	v_add_f32_e32 v27, 1.0, v27
	v_rcp_f32_e32 v27, v27
	v_med3_f32 v24, v24, s97, v176
	v_add_f32_e32 v25, v99, v7
	v_med3_f32 v25, v25, s97, v176
	v_mul_f32_e32 v20, v20, v26
	v_add_f32_e32 v24, 1.0, v24
	v_mul_f32_e32 v24, v24, v20
	v_mul_f32_e32 v20, v21, v27
	v_add_f32_e32 v21, 1.0, v25
	v_mul_f32_e32 v25, v21, v20
	v_add_f32_e32 v20, v136, v16
	v_min_f32_e32 v20, 0x40e00000, v20
	v_add_f32_e32 v21, v132, v4
	v_min_f32_e32 v21, 0x40e00000, v21
	v_mul_f32_e32 v28, 0x3fd9db23, v20
	v_mul_f32_e32 v28, 0xbfb8aa3b, v28
	v_mul_f32_e32 v29, 0x3fd9db23, v21
	v_exp_f32_e32 v28, v28
	v_mul_f32_e32 v29, 0xbfb8aa3b, v29
	v_exp_f32_e32 v29, v29
	v_add_f32_e32 v26, v104, v12
	v_add_f32_e32 v28, 1.0, v28
	v_rcp_f32_e32 v28, v28
	v_add_f32_e32 v29, 1.0, v29
	v_rcp_f32_e32 v29, v29
	v_med3_f32 v26, v26, s97, v176
	v_add_f32_e32 v27, v100, v8
	v_med3_f32 v27, v27, s97, v176
	v_mul_f32_e32 v20, v20, v28
	v_add_f32_e32 v26, 1.0, v26
	v_mul_f32_e32 v26, v26, v20
	v_mul_f32_e32 v20, v21, v29
	v_add_f32_e32 v21, 1.0, v27
	v_mul_f32_e32 v27, v21, v20
	v_add_f32_e32 v20, v137, v17
	v_min_f32_e32 v20, 0x40e00000, v20
	v_add_f32_e32 v21, v133, v5
	v_min_f32_e32 v21, 0x40e00000, v21
	v_mul_f32_e32 v30, 0x3fd9db23, v20
	v_mul_f32_e32 v30, 0xbfb8aa3b, v30
	v_mul_f32_e32 v31, 0x3fd9db23, v21
	v_exp_f32_e32 v30, v30
	v_mul_f32_e32 v31, 0xbfb8aa3b, v31
	v_exp_f32_e32 v31, v31
	v_add_f32_e32 v28, v105, v13
	v_add_f32_e32 v30, 1.0, v30
	v_rcp_f32_e32 v30, v30
	v_add_f32_e32 v31, 1.0, v31
	v_rcp_f32_e32 v31, v31
	v_med3_f32 v28, v28, s97, v176
	v_mul_f32_e32 v20, v20, v30
	v_add_f32_e32 v28, 1.0, v28
	v_mul_f32_e32 v28, v28, v20
	v_mul_f32_e32 v30, v21, v31
	v_mov_b32_e32 v20, 0
	v_mov_b32_e32 v21, 0
	v_add_f32_e32 v29, v101, v9
	v_cvt_pk_fp8_f32 v20, v22, v24
	v_cvt_pk_fp8_f32 v21, v23, v25
	v_med3_f32 v29, v29, s97, v176
	v_add_f32_e32 v22, 1.0, v29
	v_mul_f32_e32 v22, v22, v30
	v_cvt_pk_fp8_f32 v20, v26, v28 op_sel:[0,0,1]
	v_cvt_pk_fp8_f32 v21, v27, v22 op_sel:[0,0,1]
	v_add_co_u32_e32 v22, vcc, s13, v18
	s_mov_b32 s13, 0x40000
	s_nop 0
	v_addc_co_u32_e32 v23, vcc, 0, v19, vcc
	global_store_dwordx2 v[22:23], v[20:21], off
	v_add_f32_e32 v20, v94, v14
	v_min_f32_e32 v20, 0x40e00000, v20
	v_add_f32_e32 v21, v90, v2
	v_min_f32_e32 v21, 0x40e00000, v21
	v_mul_f32_e32 v24, 0x3fd9db23, v20
	v_mul_f32_e32 v24, 0xbfb8aa3b, v24
	v_mul_f32_e32 v25, 0x3fd9db23, v21
	v_exp_f32_e32 v24, v24
	v_mul_f32_e32 v25, 0xbfb8aa3b, v25
	v_exp_f32_e32 v25, v25
	v_add_f32_e32 v22, v62, v10
	v_add_f32_e32 v24, 1.0, v24
	v_rcp_f32_e32 v24, v24
	v_add_f32_e32 v25, 1.0, v25
	v_rcp_f32_e32 v25, v25
	v_med3_f32 v22, v22, s97, v176
	v_add_f32_e32 v23, v58, v6
	v_med3_f32 v23, v23, s97, v176
	v_mul_f32_e32 v20, v20, v24
	v_add_f32_e32 v22, 1.0, v22
	v_mul_f32_e32 v22, v22, v20
	v_mul_f32_e32 v20, v21, v25
	v_add_f32_e32 v21, 1.0, v23
	v_mul_f32_e32 v23, v21, v20
	v_add_f32_e32 v20, v95, v15
	v_min_f32_e32 v20, 0x40e00000, v20
	v_add_f32_e32 v21, v91, v3
	v_min_f32_e32 v21, 0x40e00000, v21
	v_mul_f32_e32 v26, 0x3fd9db23, v20
	v_mul_f32_e32 v26, 0xbfb8aa3b, v26
	v_mul_f32_e32 v27, 0x3fd9db23, v21
	v_exp_f32_e32 v26, v26
	v_mul_f32_e32 v27, 0xbfb8aa3b, v27
	v_exp_f32_e32 v27, v27
	v_add_f32_e32 v24, v63, v11
	v_add_f32_e32 v26, 1.0, v26
	v_rcp_f32_e32 v26, v26
	v_add_f32_e32 v27, 1.0, v27
	v_rcp_f32_e32 v27, v27
	v_med3_f32 v24, v24, s97, v176
	v_add_f32_e32 v25, v59, v7
	v_med3_f32 v25, v25, s97, v176
	v_mul_f32_e32 v20, v20, v26
	v_add_f32_e32 v24, 1.0, v24
	v_mul_f32_e32 v24, v24, v20
	v_mul_f32_e32 v20, v21, v27
	v_add_f32_e32 v21, 1.0, v25
	v_mul_f32_e32 v25, v21, v20
	v_add_f32_e32 v20, v96, v16
	v_min_f32_e32 v20, 0x40e00000, v20
	v_add_f32_e32 v21, v92, v4
	v_min_f32_e32 v21, 0x40e00000, v21
	v_mul_f32_e32 v28, 0x3fd9db23, v20
	v_mul_f32_e32 v28, 0xbfb8aa3b, v28
	v_mul_f32_e32 v29, 0x3fd9db23, v21
	v_exp_f32_e32 v28, v28
	v_mul_f32_e32 v29, 0xbfb8aa3b, v29
	v_exp_f32_e32 v29, v29
	v_add_f32_e32 v26, v64, v12
; __device__ __forceinline__ unsigned cvt4_fp8(float a, float b, float c, float d) { int w = 0; w = __builtin_amdgcn_cvt_pk_fp8_f32(a, b, w, false); w = __builtin_amdgcn_cvt_pk_fp8_f32(c, d, w, true); return (unsigned)w; }
; __device__ __forceinline__ float sigmoidf_(float x) { return __builtin_amdgcn_rcpf(1.0f + __expf(-x)); }
;     __device__ __forceinline__ void operator()(const Acc& acc, const Unit& u, int wr, int wc, int fr, int fq) const {
;     ...
;             for (int m = 0; m < 4; ++m) { f32x4 g0 = acc[ai][0][m][0] + bg0, g1 = acc[ai][0][m][1] + bg1, u0 = acc[ai][1][m][0] + bu0, u1 = acc[ai][1][m][1] + bu1, r0, r1;
; #pragma unroll
;                 for (int j = 0; j < 4; ++j) {
;                     const float ga = fminf(g0[j], 7.0f), gb = fminf(g1[j], 7.0f);
;                     const float ua = fminf(fmaxf(u0[j], -7.0f), 7.0f), ub = fminf(fmaxf(u1[j], -7.0f), 7.0f);
;                     r0[j] = ga * sigmoidf_(1.702f * ga) * (ua + 1.0f); r1[j] = gb * sigmoidf_(1.702f * gb) * (ub + 1.0f); }
;                 u32x2 w; w.x = cvt4_fp8(r0[0], r0[1], r0[2], r0[3]); w.y = cvt4_fp8(r1[0], r1[1], r1[2], r1[3]);
;                 *(u32x2*)(O + (size_t)(row0 + ai * HALF + m * 16) * DM + hc) = w; }
	v_add_f32_e32 v28, 1.0, v28
	v_rcp_f32_e32 v28, v28
	v_add_f32_e32 v29, 1.0, v29
	v_rcp_f32_e32 v29, v29
	v_med3_f32 v26, v26, s97, v176
	v_add_f32_e32 v27, v60, v8
	v_med3_f32 v27, v27, s97, v176
	v_mul_f32_e32 v20, v20, v28
	v_add_f32_e32 v26, 1.0, v26
	v_mul_f32_e32 v26, v26, v20
	v_mul_f32_e32 v20, v21, v29
	v_add_f32_e32 v21, 1.0, v27
	v_mul_f32_e32 v27, v21, v20
	v_add_f32_e32 v20, v97, v17
	v_min_f32_e32 v20, 0x40e00000, v20
	v_add_f32_e32 v21, v93, v5
	v_min_f32_e32 v21, 0x40e00000, v21
	v_mul_f32_e32 v30, 0x3fd9db23, v20
	v_mul_f32_e32 v30, 0xbfb8aa3b, v30
	v_mul_f32_e32 v31, 0x3fd9db23, v21
	v_exp_f32_e32 v30, v30
	v_mul_f32_e32 v31, 0xbfb8aa3b, v31
	v_exp_f32_e32 v31, v31
	v_add_f32_e32 v28, v65, v13
	v_add_f32_e32 v30, 1.0, v30
	v_rcp_f32_e32 v30, v30
	v_add_f32_e32 v31, 1.0, v31
	v_rcp_f32_e32 v31, v31
	v_med3_f32 v28, v28, s97, v176
	v_mul_f32_e32 v20, v20, v30
	v_add_f32_e32 v28, 1.0, v28
	v_mul_f32_e32 v28, v28, v20
	v_mul_f32_e32 v30, v21, v31
	v_mov_b32_e32 v20, 0
	v_mov_b32_e32 v21, 0
	v_add_f32_e32 v29, v61, v9
	v_cvt_pk_fp8_f32 v20, v22, v24
	v_cvt_pk_fp8_f32 v21, v23, v25
	v_med3_f32 v29, v29, s97, v176
	v_add_f32_e32 v22, 1.0, v29
	v_mul_f32_e32 v22, v22, v30
	v_cvt_pk_fp8_f32 v20, v26, v28 op_sel:[0,0,1]
	v_cvt_pk_fp8_f32 v21, v27, v22 op_sel:[0,0,1]
	v_add_co_u32_e32 v22, vcc, s13, v18
	s_mov_b32 s13, 0x48000
	s_nop 0
	v_addc_co_u32_e32 v23, vcc, 0, v19, vcc
	global_store_dwordx2 v[22:23], v[20:21], off
	v_add_f32_e32 v20, v86, v14
	v_min_f32_e32 v20, 0x40e00000, v20
	v_add_f32_e32 v21, v82, v2
	v_min_f32_e32 v21, 0x40e00000, v21
	v_mul_f32_e32 v24, 0x3fd9db23, v20
	v_mul_f32_e32 v24, 0xbfb8aa3b, v24
	v_mul_f32_e32 v25, 0x3fd9db23, v21
	v_exp_f32_e32 v24, v24
	v_mul_f32_e32 v25, 0xbfb8aa3b, v25
	v_exp_f32_e32 v25, v25
	v_add_f32_e32 v22, v54, v10
	v_add_f32_e32 v24, 1.0, v24
	v_rcp_f32_e32 v24, v24
	v_add_f32_e32 v25, 1.0, v25
	v_rcp_f32_e32 v25, v25
	v_med3_f32 v22, v22, s97, v176
	v_add_f32_e32 v23, v50, v6
	v_med3_f32 v23, v23, s97, v176
	v_mul_f32_e32 v20, v20, v24
	v_add_f32_e32 v22, 1.0, v22
	v_mul_f32_e32 v22, v22, v20
	v_mul_f32_e32 v20, v21, v25
	v_add_f32_e32 v21, 1.0, v23
	v_mul_f32_e32 v23, v21, v20
	v_add_f32_e32 v20, v87, v15
	v_min_f32_e32 v20, 0x40e00000, v20
	v_add_f32_e32 v21, v83, v3
	v_min_f32_e32 v21, 0x40e00000, v21
	v_mul_f32_e32 v26, 0x3fd9db23, v20
	v_mul_f32_e32 v26, 0xbfb8aa3b, v26
	v_mul_f32_e32 v27, 0x3fd9db23, v21
	v_exp_f32_e32 v26, v26
	v_mul_f32_e32 v27, 0xbfb8aa3b, v27
	v_exp_f32_e32 v27, v27
	v_add_f32_e32 v24, v55, v11
	v_add_f32_e32 v26, 1.0, v26
	v_rcp_f32_e32 v26, v26
	v_add_f32_e32 v27, 1.0, v27
	v_rcp_f32_e32 v27, v27
	v_med3_f32 v24, v24, s97, v176
	v_add_f32_e32 v25, v51, v7
	v_med3_f32 v25, v25, s97, v176
	v_mul_f32_e32 v20, v20, v26
	v_add_f32_e32 v24, 1.0, v24
	v_mul_f32_e32 v24, v24, v20
	v_mul_f32_e32 v20, v21, v27
	v_add_f32_e32 v21, 1.0, v25
	v_mul_f32_e32 v25, v21, v20
	v_add_f32_e32 v20, v88, v16
	v_min_f32_e32 v20, 0x40e00000, v20
	v_add_f32_e32 v21, v84, v4
	v_min_f32_e32 v21, 0x40e00000, v21
	v_mul_f32_e32 v28, 0x3fd9db23, v20
	v_mul_f32_e32 v28, 0xbfb8aa3b, v28
	v_mul_f32_e32 v29, 0x3fd9db23, v21
	v_exp_f32_e32 v28, v28
	v_mul_f32_e32 v29, 0xbfb8aa3b, v29
	v_exp_f32_e32 v29, v29
	v_add_f32_e32 v26, v56, v12
	v_add_f32_e32 v28, 1.0, v28
	v_rcp_f32_e32 v28, v28
	v_add_f32_e32 v29, 1.0, v29
	v_rcp_f32_e32 v29, v29
	v_med3_f32 v26, v26, s97, v176
	v_add_f32_e32 v27, v52, v8
	v_med3_f32 v27, v27, s97, v176
	v_mul_f32_e32 v20, v20, v28
	v_add_f32_e32 v26, 1.0, v26
	v_mul_f32_e32 v26, v26, v20
	v_mul_f32_e32 v20, v21, v29
	v_add_f32_e32 v21, 1.0, v27
	v_mul_f32_e32 v27, v21, v20
	v_add_f32_e32 v20, v89, v17
	v_min_f32_e32 v20, 0x40e00000, v20
	v_add_f32_e32 v21, v85, v5
	v_min_f32_e32 v21, 0x40e00000, v21
	v_mul_f32_e32 v30, 0x3fd9db23, v20
	v_mul_f32_e32 v30, 0xbfb8aa3b, v30
	v_mul_f32_e32 v31, 0x3fd9db23, v21
	v_exp_f32_e32 v30, v30
	v_mul_f32_e32 v31, 0xbfb8aa3b, v31
	v_exp_f32_e32 v31, v31
	v_add_f32_e32 v28, v57, v13
	v_add_f32_e32 v30, 1.0, v30
	v_rcp_f32_e32 v30, v30
	v_add_f32_e32 v31, 1.0, v31
	v_rcp_f32_e32 v31, v31
	v_med3_f32 v28, v28, s97, v176
	v_mul_f32_e32 v20, v20, v30
	v_add_f32_e32 v28, 1.0, v28
	v_mul_f32_e32 v28, v28, v20
	v_mul_f32_e32 v30, v21, v31
	v_mov_b32_e32 v20, 0
	v_mov_b32_e32 v21, 0
	v_add_f32_e32 v29, v53, v9
	v_cvt_pk_fp8_f32 v20, v22, v24
	v_cvt_pk_fp8_f32 v21, v23, v25
	v_med3_f32 v29, v29, s97, v176
	v_add_f32_e32 v22, 1.0, v29
	v_mul_f32_e32 v22, v22, v30
	v_cvt_pk_fp8_f32 v20, v26, v28 op_sel:[0,0,1]
	v_cvt_pk_fp8_f32 v21, v27, v22 op_sel:[0,0,1]
	v_add_co_u32_e32 v22, vcc, s13, v18
	s_mov_b32 s13, 0x50000
	s_nop 0
	v_addc_co_u32_e32 v23, vcc, 0, v19, vcc
	global_store_dwordx2 v[22:23], v[20:21], off
	v_add_f32_e32 v20, v78, v14
	v_min_f32_e32 v20, 0x40e00000, v20
	v_add_f32_e32 v21, v74, v2
	v_min_f32_e32 v21, 0x40e00000, v21
	v_mul_f32_e32 v24, 0x3fd9db23, v20
	v_mul_f32_e32 v24, 0xbfb8aa3b, v24
	v_mul_f32_e32 v25, 0x3fd9db23, v21
	v_exp_f32_e32 v24, v24
	v_mul_f32_e32 v25, 0xbfb8aa3b, v25
	v_exp_f32_e32 v25, v25
	v_add_f32_e32 v22, v46, v10
	v_add_f32_e32 v24, 1.0, v24
	v_rcp_f32_e32 v24, v24
	v_add_f32_e32 v25, 1.0, v25
	v_rcp_f32_e32 v25, v25
	v_med3_f32 v22, v22, s97, v176
	v_add_f32_e32 v23, v42, v6
	v_med3_f32 v23, v23, s97, v176
	v_mul_f32_e32 v20, v20, v24
	v_add_f32_e32 v22, 1.0, v22
	v_mul_f32_e32 v22, v22, v20
	v_mul_f32_e32 v20, v21, v25
	v_add_f32_e32 v21, 1.0, v23
	v_mul_f32_e32 v23, v21, v20
	v_add_f32_e32 v20, v79, v15
	v_min_f32_e32 v20, 0x40e00000, v20
	v_add_f32_e32 v21, v75, v3
	v_min_f32_e32 v21, 0x40e00000, v21
	v_mul_f32_e32 v26, 0x3fd9db23, v20
; __device__ __forceinline__ unsigned cvt4_fp8(float a, float b, float c, float d) { int w = 0; w = __builtin_amdgcn_cvt_pk_fp8_f32(a, b, w, false); w = __builtin_amdgcn_cvt_pk_fp8_f32(c, d, w, true); return (unsigned)w; }
; __device__ __forceinline__ float sigmoidf_(float x) { return __builtin_amdgcn_rcpf(1.0f + __expf(-x)); }
; #define PG8_BAR __builtin_amdgcn_s_barrier()
;     __device__ __forceinline__ void operator()(const Acc& acc, const Unit& u, int wr, int wc, int fr, int fq) const {
;     ...
;             for (int m = 0; m < 4; ++m) { f32x4 g0 = acc[ai][0][m][0] + bg0, g1 = acc[ai][0][m][1] + bg1, u0 = acc[ai][1][m][0] + bu0, u1 = acc[ai][1][m][1] + bu1, r0, r1;
; #pragma unroll
;                 for (int j = 0; j < 4; ++j) {
;                     const float ga = fminf(g0[j], 7.0f), gb = fminf(g1[j], 7.0f);
;                     const float ua = fminf(fmaxf(u0[j], -7.0f), 7.0f), ub = fminf(fmaxf(u1[j], -7.0f), 7.0f);
;                     r0[j] = ga * sigmoidf_(1.702f * ga) * (ua + 1.0f); r1[j] = gb * sigmoidf_(1.702f * gb) * (ub + 1.0f); }
;                 u32x2 w; w.x = cvt4_fp8(r0[0], r0[1], r0[2], r0[3]); w.y = cvt4_fp8(r1[0], r1[1], r1[2], r1[3]);
;                 *(u32x2*)(O + (size_t)(row0 + ai * HALF + m * 16) * DM + hc) = w; }
; template <class Epi, class Sched, bool F8 = false, bool MID = false, bool GATHER = false>
; __device__ __forceinline__ void gemm_phase(LAS unsigned char* lds, const Gemm g, const Sched& S, const Epi& E) {
;     ...
;         if (!has_next) break;
; #pragma unroll
;         for (int a = 0; a < 2; ++a)
; #pragma unroll
;             for (int b = 0; b < 2; ++b)
; #pragma unroll
;                 for (int m = 0; m < 4; ++m)
; #pragma unroll
;                     for (int n = 0; n < 2; ++n) acc[a][b][m][n] = (f32x4){0.f, 0.f, 0.f, 0.f};
;         cur = nxt; cA = nA; cB = nB; ++ui;
;         if constexpr (GATHER) {
; #pragma unroll
;             for (int i = 0; i < 2; ++i) { voffA[i] = nvA0[i]; voffA1[i] = nvA1[i]; } }
;         if (wr == 1) PG8_BAR;
	v_mul_f32_e32 v26, 0xbfb8aa3b, v26
	v_mul_f32_e32 v27, 0x3fd9db23, v21
	v_exp_f32_e32 v26, v26
	v_mul_f32_e32 v27, 0xbfb8aa3b, v27
	v_exp_f32_e32 v27, v27
	v_add_f32_e32 v24, v47, v11
	v_add_f32_e32 v26, 1.0, v26
	v_rcp_f32_e32 v26, v26
	v_add_f32_e32 v27, 1.0, v27
	v_rcp_f32_e32 v27, v27
	v_med3_f32 v24, v24, s97, v176
	v_add_f32_e32 v25, v43, v7
	v_med3_f32 v25, v25, s97, v176
	v_mul_f32_e32 v20, v20, v26
	v_add_f32_e32 v24, 1.0, v24
	v_mul_f32_e32 v24, v24, v20
	v_mul_f32_e32 v20, v21, v27
	v_add_f32_e32 v21, 1.0, v25
	v_mul_f32_e32 v25, v21, v20
	v_add_f32_e32 v20, v80, v16
	v_min_f32_e32 v20, 0x40e00000, v20
	v_add_f32_e32 v21, v76, v4
	v_min_f32_e32 v21, 0x40e00000, v21
	v_mul_f32_e32 v28, 0x3fd9db23, v20
	v_mul_f32_e32 v28, 0xbfb8aa3b, v28
	v_mul_f32_e32 v29, 0x3fd9db23, v21
	v_exp_f32_e32 v28, v28
	v_mul_f32_e32 v29, 0xbfb8aa3b, v29
	v_exp_f32_e32 v29, v29
	v_add_f32_e32 v26, v48, v12
	v_add_f32_e32 v28, 1.0, v28
	v_rcp_f32_e32 v28, v28
	v_add_f32_e32 v29, 1.0, v29
	v_rcp_f32_e32 v29, v29
	v_med3_f32 v26, v26, s97, v176
	v_add_f32_e32 v27, v44, v8
	v_med3_f32 v27, v27, s97, v176
	v_mul_f32_e32 v20, v20, v28
	v_add_f32_e32 v26, 1.0, v26
	v_mul_f32_e32 v26, v26, v20
	v_mul_f32_e32 v20, v21, v29
	v_add_f32_e32 v21, 1.0, v27
	v_mul_f32_e32 v27, v21, v20
	v_add_f32_e32 v20, v81, v17
	v_min_f32_e32 v20, 0x40e00000, v20
	v_add_f32_e32 v21, v77, v5
	v_min_f32_e32 v21, 0x40e00000, v21
	v_mul_f32_e32 v30, 0x3fd9db23, v20
	v_mul_f32_e32 v30, 0xbfb8aa3b, v30
	v_mul_f32_e32 v31, 0x3fd9db23, v21
	v_exp_f32_e32 v30, v30
	v_mul_f32_e32 v31, 0xbfb8aa3b, v31
	v_exp_f32_e32 v31, v31
	v_add_f32_e32 v28, v49, v13
	v_add_f32_e32 v30, 1.0, v30
	v_rcp_f32_e32 v30, v30
	v_add_f32_e32 v31, 1.0, v31
	v_rcp_f32_e32 v31, v31
	v_med3_f32 v28, v28, s97, v176
	v_mul_f32_e32 v20, v20, v30
	v_add_f32_e32 v28, 1.0, v28
	v_mul_f32_e32 v28, v28, v20
	v_mul_f32_e32 v30, v21, v31
	v_mov_b32_e32 v20, 0
	v_mov_b32_e32 v21, 0
	v_add_f32_e32 v29, v45, v9
	v_cvt_pk_fp8_f32 v20, v22, v24
	v_cvt_pk_fp8_f32 v21, v23, v25
	v_med3_f32 v29, v29, s97, v176
	v_add_f32_e32 v22, 1.0, v29
	v_mul_f32_e32 v22, v22, v30
	v_cvt_pk_fp8_f32 v20, v26, v28 op_sel:[0,0,1]
	v_cvt_pk_fp8_f32 v21, v27, v22 op_sel:[0,0,1]
	v_add_co_u32_e32 v22, vcc, s13, v18
	v_add_f32_e32 v2, v66, v2
	s_nop 0
	v_addc_co_u32_e32 v23, vcc, 0, v19, vcc
	v_min_f32_e32 v2, 0x40e00000, v2
	global_store_dwordx2 v[22:23], v[20:21], off
	v_add_f32_e32 v14, v70, v14
	v_mul_f32_e32 v21, 0x3fd9db23, v2
	v_min_f32_e32 v14, 0x40e00000, v14
	v_mul_f32_e32 v21, 0xbfb8aa3b, v21
	v_mul_f32_e32 v20, 0x3fd9db23, v14
	v_exp_f32_e32 v21, v21
	v_mul_f32_e32 v20, 0xbfb8aa3b, v20
	v_exp_f32_e32 v20, v20
	v_add_f32_e32 v6, v34, v6
	v_add_f32_e32 v21, 1.0, v21
	v_rcp_f32_e32 v21, v21
	v_add_f32_e32 v20, 1.0, v20
	v_rcp_f32_e32 v20, v20
	v_med3_f32 v6, v6, s97, v176
	v_add_f32_e32 v10, v38, v10
	v_mul_f32_e32 v2, v2, v21
	v_add_f32_e32 v6, 1.0, v6
	v_med3_f32 v10, v10, s97, v176
	v_mul_f32_e32 v6, v6, v2
	v_add_f32_e32 v2, v71, v15
	v_mul_f32_e32 v14, v14, v20
	v_add_f32_e32 v10, 1.0, v10
	v_min_f32_e32 v2, 0x40e00000, v2
	v_add_f32_e32 v3, v67, v3
	v_mul_f32_e32 v10, v10, v14
	v_min_f32_e32 v3, 0x40e00000, v3
	v_mul_f32_e32 v14, 0x3fd9db23, v2
	v_mul_f32_e32 v14, 0xbfb8aa3b, v14
	v_mul_f32_e32 v15, 0x3fd9db23, v3
	v_exp_f32_e32 v14, v14
	v_mul_f32_e32 v15, 0xbfb8aa3b, v15
	v_exp_f32_e32 v15, v15
	v_add_f32_e32 v11, v39, v11
	v_add_f32_e32 v14, 1.0, v14
	v_rcp_f32_e32 v14, v14
	v_add_f32_e32 v15, 1.0, v15
	v_rcp_f32_e32 v15, v15
	v_med3_f32 v11, v11, s97, v176
	v_add_f32_e32 v7, v35, v7
	v_med3_f32 v7, v7, s97, v176
	v_mul_f32_e32 v2, v2, v14
	v_add_f32_e32 v11, 1.0, v11
	v_mul_f32_e32 v11, v11, v2
	v_mul_f32_e32 v2, v3, v15
	v_add_f32_e32 v3, 1.0, v7
	v_mul_f32_e32 v7, v3, v2
	v_add_f32_e32 v2, v72, v16
	v_min_f32_e32 v2, 0x40e00000, v2
	v_add_f32_e32 v3, v68, v4
	v_min_f32_e32 v3, 0x40e00000, v3
	v_add_f32_e32 v4, v40, v12
	v_mul_f32_e32 v12, 0x3fd9db23, v2
	v_mul_f32_e32 v12, 0xbfb8aa3b, v12
	v_mul_f32_e32 v14, 0x3fd9db23, v3
	v_exp_f32_e32 v12, v12
	v_mul_f32_e32 v14, 0xbfb8aa3b, v14
	v_exp_f32_e32 v14, v14
	v_med3_f32 v4, v4, s97, v176
	v_add_f32_e32 v12, 1.0, v12
	v_rcp_f32_e32 v12, v12
	v_add_f32_e32 v14, 1.0, v14
	v_rcp_f32_e32 v14, v14
	v_add_f32_e32 v8, v36, v8
	v_med3_f32 v8, v8, s97, v176
	v_mul_f32_e32 v2, v2, v12
	v_add_f32_e32 v4, 1.0, v4
	v_mul_f32_e32 v4, v4, v2
	v_mul_f32_e32 v2, v3, v14
	v_add_f32_e32 v3, 1.0, v8
	v_mul_f32_e32 v8, v3, v2
	v_add_f32_e32 v2, v73, v17
	v_min_f32_e32 v2, 0x40e00000, v2
	v_add_f32_e32 v3, v69, v5
	v_min_f32_e32 v3, 0x40e00000, v3
	v_mul_f32_e32 v12, 0x3fd9db23, v2
	v_add_f32_e32 v5, v41, v13
	v_mul_f32_e32 v12, 0xbfb8aa3b, v12
	v_mul_f32_e32 v13, 0x3fd9db23, v3
	v_exp_f32_e32 v12, v12
	v_mul_f32_e32 v13, 0xbfb8aa3b, v13
	v_exp_f32_e32 v13, v13
	v_med3_f32 v5, v5, s97, v176
	v_add_f32_e32 v12, 1.0, v12
	v_rcp_f32_e32 v12, v12
	v_add_f32_e32 v13, 1.0, v13
	v_rcp_f32_e32 v13, v13
	v_add_f32_e32 v5, 1.0, v5
	v_mul_f32_e32 v2, v2, v12
	v_mul_f32_e32 v5, v5, v2
	v_mul_f32_e32 v12, v3, v13
	v_mov_b32_e32 v2, 0
	v_mov_b32_e32 v3, 0
	v_add_f32_e32 v9, v37, v9
	v_cvt_pk_fp8_f32 v2, v10, v11
	v_cvt_pk_fp8_f32 v3, v6, v7
	v_med3_f32 v9, v9, s97, v176
	v_add_f32_e32 v6, 1.0, v9
	v_mul_f32_e32 v6, v6, v12
	v_cvt_pk_fp8_f32 v2, v4, v5 op_sel:[0,0,1]
	v_cvt_pk_fp8_f32 v3, v8, v6 op_sel:[0,0,1]
	v_add_co_u32_e32 v4, vcc, 0x58000, v18
	s_nop 1
	v_addc_co_u32_e32 v5, vcc, 0, v19, vcc
	s_and_b64 vcc, exec, s[4:5]
	global_store_dwordx2 v[4:5], v[2:3], off
	s_cbranch_vccnz .LBB0_2462
	s_andn2_b64 vcc, exec, s[48:49]
	s_cbranch_vccnz .LBB0_2461
	s_barrier
	s_branch .LBB0_2461

; #define LAS __attribute__((address_space(3)))
; #define PG8_STAGE(bufoff, gbase, voff) do { _Pragma("unroll") for (int _i = 0; _i < 2; ++_i) \
;         asm volatile("s_mov_b32 m0, %0\n\ts_nop 0\n\tglobal_load_lds_dwordx4 %1, %2" :: "s"(ldsb + (unsigned)(bufoff) + ldsw + _i * 8192u), "v"((voff)[_i]), "s"((const char*)(gbase)) : "m0", "memory"); } while (0)
; #define PG8_WAIT_V(n) asm volatile("s_waitcnt vmcnt(" #n ")" ::: "memory")
; #define PG8_BAR __builtin_amdgcn_s_barrier()
; template <class Epi, class Sched, bool F8 = false, bool MID = false, bool GATHER = false>
; __device__ __forceinline__ void gemm_phase(LAS unsigned char* lds, const Gemm g, const Sched& S, const Epi& E) {
;     ...
;     const unsigned ldsw = (unsigned)wid * 1024u, ldsb = (unsigned)(uintptr_t)lds;
;     const int aoff = lds_byte(wr * 64 + fr, fq * 8), boff = lds_byte(wc * 32 + fr, fq * 8);
;     ...
;     Unit cur, nxt; int ui = 0;
;     if (!S.next(0, cur)) return;
;     LAS int* rt = (LAS int*)(lds + STAGE_BYTES);
;     if constexpr (GATHER) { Unit uu;
;         for (int i = 0; i < 20 && S.next(i, uu); ++i) if (tid < 256) { const int l_ = uu.row0 - g.tab[uu.e] + tid; rt[i * 256 + tid] = l_ < g.tab[32 + uu.e] ? g.list[uu.e * T + l_] : T; }
;         asm volatile("s_waitcnt vmcnt(0) lgkmcnt(0)" ::: "memory"); __builtin_amdgcn_s_barrier(); asm volatile("" ::: "memory");
; #pragma unroll
;         for (int i = 0; i < 2; ++i) { voffA[i] = (unsigned)(rt[RA[i]] * g.lda + CA[i]); voffA1[i] = (unsigned)(rt[HALF + RA[i]] * g.lda + CA[i]); } }
;     f32x4 acc[2][2][4][2];
; #pragma unroll
;     for (int a = 0; a < 2; ++a)
; #pragma unroll
;         for (int b = 0; b < 2; ++b)
; #pragma unroll
;             for (int m = 0; m < 4; ++m)
; #pragma unroll
;                 for (int n = 0; n < 2; ++n) acc[a][b][m][n] = (f32x4){0.f, 0.f, 0.f, 0.f};
;     bf16x8 At[4][2], B0[2][2], B1[2][2]; i32x8 At8[4], B08[2], B18[2];
;     const char* cA = cur.A; const char* cB = cur.B;
;     PG8_STAGE(PG8_SB(0, 0), cB, voffB); PG8_STAGE(PG8_SB(0, 1), cB + hstepB, voffB); PG8_STAGE(PG8_SA(0, 0), cA, voffA); PG8_STAGE(PG8_SA(0, 1), cA, voffA1);
;     if (wr == 1) PG8_BAR;
;     PG8_WAIT_V(2); PG8_BAR;
;     PG8_STAGE(PG8_SB(1, 0), cB + kstep, voffB); PG8_STAGE(PG8_SA(1, 0), cA + kstep, voffA); PG8_STAGE(PG8_SB(1, 1), cB + hstepB + kstep, voffB);
;     PG8_WAIT_V(6); PG8_BAR;
.LBB0_2551:
	v_and_b32_e32 v2, 48, v0
	v_lshlrev_b32_e32 v4, 6, v0
	s_movk_i32 s13, 0x3c0
	s_lshl_b32 s96, s12, 8
	s_lshl_b32 s12, s35, 13
	v_and_b32_e32 v3, 32, v166
	v_and_or_b32 v2, v4, s13, v2
	v_bitop3_b32 v4, v2, s12, v3 bitop3:0xde
	s_lshl_b32 s12, s48, 5
	s_and_b32 s78, s12, 0x60
	s_lshl_b32 s63, s16, 8
	s_lshl_b32 s77, s35, 6
	s_lshl_b32 s12, s78, 7
	s_add_i32 s80, s17, 0x18000
	v_bitop3_b32 v2, s12, v2, v3 bitop3:0xf6
	s_add_u32 s12, s64, 0x80
	s_waitcnt vmcnt(2)
	s_barrier
	s_addc_u32 s13, s65, 0
	s_mov_b32 m0, s80
	s_nop 0
	global_load_lds_dwordx4 v163, s[12:13]
	s_add_i32 s81, s17, 0x1a000
	s_add_i32 s85, s17, 0x8000
	s_mov_b32 m0, s81
	s_nop 0
	global_load_lds_dwordx4 v168, s[12:13]
	s_add_u32 s12, s66, 0x80
	s_addc_u32 s13, s67, 0
	s_mov_b32 m0, s85
	s_nop 0
	global_load_lds_dwordx4 v1, s[12:13]
	s_add_i32 s86, s17, 0xa000
	s_add_i32 s87, s17, 0x1c000
	s_mov_b32 m0, s86
	s_nop 0
	global_load_lds_dwordx4 v165, s[12:13]
	s_add_u32 s12, s64, 0x40080
	s_addc_u32 s13, s65, 0
	s_mov_b32 m0, s87
	s_nop 0
	global_load_lds_dwordx4 v163, s[12:13]
	s_add_i32 s88, s17, 0x1e000
	s_mov_b32 m0, s88
	s_nop 0
	global_load_lds_dwordx4 v168, s[12:13]
	s_waitcnt vmcnt(6)
	s_add_i32 s89, s17, 0xc000
	s_cmpk_lt_u32 s34, 0x100
	v_add_u32_e32 v2, 0, v2
	s_mov_b32 s79, 0
	s_cselect_b64 s[12:13], -1, 0
	s_add_i32 s90, s17, 0xe000
	v_add_u32_e32 v169, 0x10000, v2
	v_add_u32_e32 v170, 0x14000, v2
	v_add_u32_e32 v171, 0, v4
	v_mov_b32_e32 v172, 0x79797979
	v_mov_b32_e32 v173, 0x7f7f7f7f
	v_add_u32_e32 v174, 0x18000, v2
	v_add_u32_e32 v175, 0x1c000, v2
	s_mov_b32 s16, 0x41000000
	s_mov_b64 s[34:35], 0x18000
	s_mov_b64 s[48:49], 0x48000
	s_mov_b32 s91, 0x48000
	s_mov_b64 s[50:51], 0x50000
	s_mov_b32 s92, 0x50000
	s_mov_b64 s[52:53], 0x58000
	s_mov_b32 s93, 0x58000
	s_mov_b64 s[58:59], s[64:65]
	s_mov_b64 s[56:57], s[66:67]
	s_barrier
	s_mov_b32 s101, 0
	s_branch .LBB0_2554

; __device__ __forceinline__ unsigned cvt4_fp8(float a, float b, float c, float d) { int w = 0; w = __builtin_amdgcn_cvt_pk_fp8_f32(a, b, w, false); w = __builtin_amdgcn_cvt_pk_fp8_f32(c, d, w, true); return (unsigned)w; }
;     __device__ __forceinline__ void operator()(const Acc& acc, const Unit& u, int wr, int wc, int fr, int fq) const {
;         const int row0 = u.row0 + wr * 64 + fr, col0 = u.col0 + wc * 32 + 8 * fq;
;         const float* bp = bd + (size_t)u.e * DM + col0;
;         f32x4 bv[2][2];
; #pragma unroll
;         for (int bj = 0; bj < 2; ++bj) { bv[bj][0] = *(const f32x4*)(bp + bj * HALF); bv[bj][1] = *(const f32x4*)(bp + bj * HALF + 4); }
; #pragma unroll
;         for (int ai = 0; ai < 2; ++ai)
; #pragma unroll
;             for (int m = 0; m < 4; ++m) { unsigned char* rowp = O + (size_t)(row0 + ai * HALF + m * 16) * DM + col0;
; #pragma unroll
;                 for (int bj = 0; bj < 2; ++bj) { const f32x4 y0 = (acc[ai][bj][m][0] + bv[bj][0]) * 8.0f, y1 = (acc[ai][bj][m][1] + bv[bj][1]) * 8.0f;
;                     u32x2 w; w.x = cvt4_fp8(y0[0], y0[1], y0[2], y0[3]); w.y = cvt4_fp8(y1[0], y1[1], y1[2], y1[3]); *(u32x2*)(rowp + bj * HALF) = w; } }
.LBB0_2560:
	s_nop 15
	s_nop 15
	v_mbcnt_lo_u32_b32 v30, -1, 0
	v_mbcnt_hi_u32_b32 v30, -1, v30
	s_add_i32 s22, s63, s78
	v_ashrrev_i32_e32 v2, 1, v30
	v_and_b32_e32 v2, -8, v2
	s_ashr_i32 s63, s62, 31
	v_add_u32_e32 v18, s22, v2
	s_lshl_b64 s[22:23], s[62:63], 13
	s_add_u32 s22, s4, s22
	s_addc_u32 s23, s5, s23
	v_ashrrev_i32_e32 v19, 31, v18
	v_lshl_add_u64 v[2:3], v[18:19], 2, s[22:23]
	s_cmp_lg_u32 s101, 0
	s_cbranch_scc1 .Lb11_have
	global_load_dwordx4 v[14:17], v[2:3], off
	global_load_dwordx4 v[10:13], v[2:3], off offset:16
	global_load_dwordx4 v[6:9], v[2:3], off offset:512
	s_nop 0
	global_load_dwordx4 v[2:5], v[2:3], off offset:528
	s_branch .Lb11_join
.Lb11_have:
	v_mov_b32_e32 v14, v218
	v_mov_b32_e32 v15, v219
	v_mov_b32_e32 v16, v220
	v_mov_b32_e32 v17, v221
	v_mov_b32_e32 v10, v222
	v_mov_b32_e32 v11, v223
	v_mov_b32_e32 v12, v224
	v_mov_b32_e32 v13, v225
	v_mov_b32_e32 v6, v226
	v_mov_b32_e32 v7, v227
	v_mov_b32_e32 v8, v228
	v_mov_b32_e32 v9, v229
	v_mov_b32_e32 v2, v230
	v_mov_b32_e32 v3, v231
	v_mov_b32_e32 v4, v232
	v_mov_b32_e32 v5, v233
.Lb11_join:
	v_mov_b32_e32 v20, 0
	v_mov_b32_e32 v21, 0
	v_mov_b32_e32 v22, 0
	v_mov_b32_e32 v23, 0
	v_mov_b32_e32 v24, 0
	v_mov_b32_e32 v25, 0
	v_and_or_b32 v30, v30, 15, s77
	v_mov_b32_e32 v26, 0
	v_mov_b32_e32 v27, 0
	v_add_u32_e32 v30, s96, v30
	v_ashrrev_i32_e32 v31, 31, v30
	v_lshlrev_b64 v[30:31], 11, v[30:31]
	v_lshl_add_u64 v[30:31], s[28:29], 0, v[30:31]
	s_mov_b32 s55, 0x8000
	v_lshl_add_u64 v[18:19], v[30:31], 0, v[18:19]
	v_mov_b32_e32 v29, 0
	s_mov_b64 s[22:23], 0x8000
	v_add_co_u32_e32 v32, vcc, s55, v18
	v_mov_b32_e32 v28, 0
	v_lshl_add_u64 v[30:31], v[18:19], 0, s[22:23]
	v_addc_co_u32_e32 v33, vcc, 0, v19, vcc
	s_mov_b32 s22, 0x10000
	s_mov_b64 s[62:63], 0x10000
	v_lshl_add_u64 v[176:177], v[18:19], 0, s[62:63]
	s_waitcnt vmcnt(3)
	v_pk_add_f32 v[158:159], v[158:159], v[14:15]
	s_waitcnt vmcnt(2)
	v_pk_add_f32 v[154:155], v[154:155], v[10:11]
	s_waitcnt vmcnt(1)
	v_pk_add_f32 v[138:139], v[138:139], v[6:7]
	s_waitcnt vmcnt(0)
	s_mov_b32 s101, 0
	s_andn2_b64 vcc, exec, s[60:61]
	s_cbranch_vccnz .Lb11_nonext
	s_add_i32 s98, s95, s78
	s_lshl_b32 s99, s54, 13
	v_mbcnt_lo_u32_b32 v248, -1, 0
	v_mbcnt_hi_u32_b32 v248, -1, v248
	v_ashrrev_i32_e32 v248, 1, v248
	v_and_b32_e32 v248, -8, v248
	v_add_u32_e32 v248, s98, v248
	v_lshl_add_u32 v248, v248, 2, s99
	global_load_dwordx4 v[218:221], v248, s[4:5]
	global_load_dwordx4 v[222:225], v248, s[4:5] offset:16
	global_load_dwordx4 v[226:229], v248, s[4:5] offset:512
	global_load_dwordx4 v[230:233], v248, s[4:5] offset:528
	s_mov_b32 s101, 1
.Lb11_nonext:
	v_pk_add_f32 v[134:135], v[134:135], v[2:3]
	v_pk_mul_f32 v[158:159], v[158:159], s[16:17] op_sel_hi:[1,0]
	v_pk_mul_f32 v[154:155], v[154:155], s[16:17] op_sel_hi:[1,0]
	v_pk_add_f32 v[150:151], v[150:151], v[14:15]
	v_pk_add_f32 v[146:147], v[146:147], v[10:11]
	v_pk_mul_f32 v[138:139], v[138:139], s[16:17] op_sel_hi:[1,0]
	v_pk_mul_f32 v[134:135], v[134:135], s[16:17] op_sel_hi:[1,0]
	v_cvt_pk_fp8_f32 v20, v158, v159
	v_cvt_pk_fp8_f32 v21, v154, v155
	v_pk_add_f32 v[130:131], v[130:131], v[6:7]
	v_pk_add_f32 v[126:127], v[126:127], v[2:3]
	v_pk_mul_f32 v[150:151], v[150:151], s[16:17] op_sel_hi:[1,0]
	v_pk_mul_f32 v[146:147], v[146:147], s[16:17] op_sel_hi:[1,0]
	v_cvt_pk_fp8_f32 v22, v138, v139
	v_cvt_pk_fp8_f32 v23, v134, v135
	v_pk_add_f32 v[160:161], v[160:161], v[16:17]
	v_pk_add_f32 v[156:157], v[156:157], v[12:13]
	v_pk_mul_f32 v[130:131], v[130:131], s[16:17] op_sel_hi:[1,0]
	v_pk_mul_f32 v[126:127], v[126:127], s[16:17] op_sel_hi:[1,0]
	v_cvt_pk_fp8_f32 v24, v150, v151
	v_cvt_pk_fp8_f32 v25, v146, v147
	v_pk_add_f32 v[140:141], v[140:141], v[8:9]
	v_pk_add_f32 v[136:137], v[136:137], v[4:5]
	v_pk_mul_f32 v[160:161], v[160:161], s[16:17] op_sel_hi:[1,0]
	v_pk_mul_f32 v[156:157], v[156:157], s[16:17] op_sel_hi:[1,0]
	v_cvt_pk_fp8_f32 v26, v130, v131
	v_cvt_pk_fp8_f32 v27, v126, v127
	v_pk_add_f32 v[152:153], v[152:153], v[16:17]
	v_pk_add_f32 v[148:149], v[148:149], v[12:13]
	v_pk_mul_f32 v[140:141], v[140:141], s[16:17] op_sel_hi:[1,0]
	v_pk_mul_f32 v[136:137], v[136:137], s[16:17] op_sel_hi:[1,0]
	v_cvt_pk_fp8_f32 v20, v160, v161 op_sel:[0,0,1]
	v_cvt_pk_fp8_f32 v21, v156, v157 op_sel:[0,0,1]
	v_pk_add_f32 v[132:133], v[132:133], v[8:9]
	v_pk_add_f32 v[128:129], v[128:129], v[4:5]
	v_pk_mul_f32 v[152:153], v[152:153], s[16:17] op_sel_hi:[1,0]
	v_pk_mul_f32 v[148:149], v[148:149], s[16:17] op_sel_hi:[1,0]
	v_cvt_pk_fp8_f32 v22, v140, v141 op_sel:[0,0,1]
	v_cvt_pk_fp8_f32 v23, v136, v137 op_sel:[0,0,1]
	v_pk_add_f32 v[122:123], v[122:123], v[10:11]
	v_pk_mul_f32 v[132:133], v[132:133], s[16:17] op_sel_hi:[1,0]
	v_pk_mul_f32 v[128:129], v[128:129], s[16:17] op_sel_hi:[1,0]
	v_cvt_pk_fp8_f32 v24, v152, v153 op_sel:[0,0,1]
	v_cvt_pk_fp8_f32 v25, v148, v149 op_sel:[0,0,1]
	v_pk_add_f32 v[142:143], v[142:143], v[14:15]
	v_pk_mul_f32 v[122:123], v[122:123], s[16:17] op_sel_hi:[1,0]
	v_cvt_pk_fp8_f32 v26, v132, v133 op_sel:[0,0,1]
	v_cvt_pk_fp8_f32 v27, v128, v129 op_sel:[0,0,1]
	v_pk_mul_f32 v[142:143], v[142:143], s[16:17] op_sel_hi:[1,0]
	global_store_dwordx2 v[18:19], v[20:21], off
	global_store_dwordx2 v[18:19], v[22:23], off offset:128
	global_store_dwordx2 v[32:33], v[24:25], off
	global_store_dwordx2 v[30:31], v[26:27], off offset:128
	v_cvt_pk_fp8_f32 v29, v122, v123
	v_pk_add_f32 v[22:23], v[118:119], v[6:7]
	v_pk_add_f32 v[24:25], v[110:111], v[2:3]
	v_cvt_pk_fp8_f32 v28, v142, v143
	v_pk_mul_f32 v[22:23], v[22:23], s[16:17] op_sel_hi:[1,0]
	v_pk_mul_f32 v[24:25], v[24:25], s[16:17] op_sel_hi:[1,0]
	v_mov_b32_e32 v26, 0
	v_mov_b32_e32 v27, 0
; __device__ __forceinline__ unsigned cvt4_fp8(float a, float b, float c, float d) { int w = 0; w = __builtin_amdgcn_cvt_pk_fp8_f32(a, b, w, false); w = __builtin_amdgcn_cvt_pk_fp8_f32(c, d, w, true); return (unsigned)w; }
;     __device__ __forceinline__ void operator()(const Acc& acc, const Unit& u, int wr, int wc, int fr, int fq) const {
;     ...
;             for (int m = 0; m < 4; ++m) { unsigned char* rowp = O + (size_t)(row0 + ai * HALF + m * 16) * DM + col0;
; #pragma unroll
;                 for (int bj = 0; bj < 2; ++bj) { const f32x4 y0 = (acc[ai][bj][m][0] + bv[bj][0]) * 8.0f, y1 = (acc[ai][bj][m][1] + bv[bj][1]) * 8.0f;
;                     u32x2 w; w.x = cvt4_fp8(y0[0], y0[1], y0[2], y0[3]); w.y = cvt4_fp8(y1[0], y1[1], y1[2], y1[3]); *(u32x2*)(rowp + bj * HALF) = w; } }
	v_pk_add_f32 v[20:21], v[124:125], v[12:13]
	v_cvt_pk_fp8_f32 v26, v22, v23
	v_cvt_pk_fp8_f32 v27, v24, v25
	v_pk_add_f32 v[144:145], v[144:145], v[16:17]
	v_pk_mul_f32 v[20:21], v[20:21], s[16:17] op_sel_hi:[1,0]
	v_pk_mul_f32 v[144:145], v[144:145], s[16:17] op_sel_hi:[1,0]
	v_cvt_pk_fp8_f32 v29, v20, v21 op_sel:[0,0,1]
	v_pk_add_f32 v[20:21], v[120:121], v[8:9]
	v_pk_add_f32 v[22:23], v[112:113], v[4:5]
	v_cvt_pk_fp8_f32 v28, v144, v145 op_sel:[0,0,1]
	v_pk_mul_f32 v[20:21], v[20:21], s[16:17] op_sel_hi:[1,0]
	v_pk_mul_f32 v[22:23], v[22:23], s[16:17] op_sel_hi:[1,0]
	v_cvt_pk_fp8_f32 v26, v20, v21 op_sel:[0,0,1]
	v_cvt_pk_fp8_f32 v27, v22, v23 op_sel:[0,0,1]
	v_add_co_u32_e32 v20, vcc, s22, v18
	v_pk_add_f32 v[24:25], v[114:115], v[14:15]
	s_nop 0
	v_addc_co_u32_e32 v21, vcc, 0, v19, vcc
	global_store_dwordx2 v[20:21], v[28:29], off
	global_store_dwordx2 v[176:177], v[26:27], off offset:128
	v_pk_add_f32 v[26:27], v[106:107], v[10:11]
	v_mov_b32_e32 v29, 0
	v_pk_mul_f32 v[26:27], v[26:27], s[16:17] op_sel_hi:[1,0]
	v_pk_mul_f32 v[24:25], v[24:25], s[16:17] op_sel_hi:[1,0]
	v_cvt_pk_fp8_f32 v29, v26, v27
	v_mov_b32_e32 v28, 0
	v_cvt_pk_fp8_f32 v28, v24, v25
	v_pk_add_f32 v[24:25], v[108:109], v[12:13]
	v_pk_add_f32 v[26:27], v[98:99], v[2:3]
	v_pk_mul_f32 v[24:25], v[24:25], s[16:17] op_sel_hi:[1,0]
	v_pk_mul_f32 v[26:27], v[26:27], s[16:17] op_sel_hi:[1,0]
	v_cvt_pk_fp8_f32 v29, v24, v25 op_sel:[0,0,1]
	v_pk_add_f32 v[24:25], v[102:103], v[6:7]
	v_mov_b32_e32 v30, 0
	v_pk_mul_f32 v[24:25], v[24:25], s[16:17] op_sel_hi:[1,0]
	v_mov_b32_e32 v31, 0
	v_pk_add_f32 v[22:23], v[116:117], v[16:17]
	v_cvt_pk_fp8_f32 v30, v24, v25
	v_cvt_pk_fp8_f32 v31, v26, v27
	v_pk_mul_f32 v[22:23], v[22:23], s[16:17] op_sel_hi:[1,0]
	v_pk_add_f32 v[24:25], v[100:101], v[4:5]
	v_cvt_pk_fp8_f32 v28, v22, v23 op_sel:[0,0,1]
	v_pk_add_f32 v[22:23], v[104:105], v[8:9]
	v_pk_mul_f32 v[24:25], v[24:25], s[16:17] op_sel_hi:[1,0]
	v_pk_mul_f32 v[22:23], v[22:23], s[16:17] op_sel_hi:[1,0]
	v_cvt_pk_fp8_f32 v31, v24, v25 op_sel:[0,0,1]
	v_cvt_pk_fp8_f32 v30, v22, v23 op_sel:[0,0,1]
	s_mov_b32 s22, 0x18000
	v_add_co_u32_e32 v22, vcc, s22, v18
	v_pk_add_f32 v[26:27], v[90:91], v[10:11]
	s_nop 0
	v_addc_co_u32_e32 v23, vcc, 0, v19, vcc
	v_lshl_add_u64 v[20:21], v[18:19], 0, s[34:35]
	global_store_dwordx2 v[22:23], v[28:29], off
	global_store_dwordx2 v[20:21], v[30:31], off offset:128
	v_pk_mul_f32 v[26:27], v[26:27], s[16:17] op_sel_hi:[1,0]
	v_mov_b32_e32 v29, 0
	v_pk_add_f32 v[24:25], v[94:95], v[14:15]
	v_cvt_pk_fp8_f32 v29, v26, v27
	v_pk_mul_f32 v[24:25], v[24:25], s[16:17] op_sel_hi:[1,0]
	v_mov_b32_e32 v28, 0
	v_cvt_pk_fp8_f32 v28, v24, v25
	v_pk_add_f32 v[24:25], v[92:93], v[12:13]
	v_pk_add_f32 v[26:27], v[78:79], v[2:3]
	v_pk_mul_f32 v[24:25], v[24:25], s[16:17] op_sel_hi:[1,0]
	v_pk_mul_f32 v[26:27], v[26:27], s[16:17] op_sel_hi:[1,0]
	v_cvt_pk_fp8_f32 v29, v24, v25 op_sel:[0,0,1]
	v_pk_add_f32 v[24:25], v[86:87], v[6:7]
	v_mov_b32_e32 v30, 0
	v_pk_mul_f32 v[24:25], v[24:25], s[16:17] op_sel_hi:[1,0]
	v_mov_b32_e32 v31, 0
	v_pk_add_f32 v[22:23], v[96:97], v[16:17]
	v_cvt_pk_fp8_f32 v30, v24, v25
	v_cvt_pk_fp8_f32 v31, v26, v27
	v_pk_mul_f32 v[22:23], v[22:23], s[16:17] op_sel_hi:[1,0]
	v_pk_add_f32 v[24:25], v[80:81], v[4:5]
	v_cvt_pk_fp8_f32 v28, v22, v23 op_sel:[0,0,1]
	v_pk_add_f32 v[22:23], v[88:89], v[8:9]
	s_mov_b64 s[22:23], 0x40000
	v_pk_mul_f32 v[22:23], v[22:23], s[16:17] op_sel_hi:[1,0]
	v_pk_mul_f32 v[24:25], v[24:25], s[16:17] op_sel_hi:[1,0]
	v_lshl_add_u64 v[20:21], v[18:19], 0, s[22:23]
	v_cvt_pk_fp8_f32 v30, v22, v23 op_sel:[0,0,1]
	v_cvt_pk_fp8_f32 v31, v24, v25 op_sel:[0,0,1]
	s_mov_b32 s22, 0x40000
	v_add_co_u32_e32 v22, vcc, s22, v18
	v_pk_add_f32 v[26:27], v[70:71], v[10:11]
	s_nop 0
	v_addc_co_u32_e32 v23, vcc, 0, v19, vcc
	global_store_dwordx2 v[22:23], v[28:29], off
	global_store_dwordx2 v[20:21], v[30:31], off offset:128
	v_pk_mul_f32 v[26:27], v[26:27], s[16:17] op_sel_hi:[1,0]
	v_mov_b32_e32 v29, 0
	v_pk_add_f32 v[24:25], v[82:83], v[14:15]
	v_cvt_pk_fp8_f32 v29, v26, v27
	v_pk_mul_f32 v[24:25], v[24:25], s[16:17] op_sel_hi:[1,0]
	v_mov_b32_e32 v28, 0
	v_cvt_pk_fp8_f32 v28, v24, v25
; __device__ __forceinline__ unsigned cvt4_fp8(float a, float b, float c, float d) { int w = 0; w = __builtin_amdgcn_cvt_pk_fp8_f32(a, b, w, false); w = __builtin_amdgcn_cvt_pk_fp8_f32(c, d, w, true); return (unsigned)w; }
; #define PG8_BAR __builtin_amdgcn_s_barrier()
;     __device__ __forceinline__ void operator()(const Acc& acc, const Unit& u, int wr, int wc, int fr, int fq) const {
;     ...
;             for (int m = 0; m < 4; ++m) { unsigned char* rowp = O + (size_t)(row0 + ai * HALF + m * 16) * DM + col0;
; #pragma unroll
;                 for (int bj = 0; bj < 2; ++bj) { const f32x4 y0 = (acc[ai][bj][m][0] + bv[bj][0]) * 8.0f, y1 = (acc[ai][bj][m][1] + bv[bj][1]) * 8.0f;
;                     u32x2 w; w.x = cvt4_fp8(y0[0], y0[1], y0[2], y0[3]); w.y = cvt4_fp8(y1[0], y1[1], y1[2], y1[3]); *(u32x2*)(rowp + bj * HALF) = w; } }
; template <class Epi, class Sched, bool F8 = false, bool MID = false, bool GATHER = false>
; __device__ __forceinline__ void gemm_phase(LAS unsigned char* lds, const Gemm g, const Sched& S, const Epi& E) {
;     ...
;         if (!has_next) break;
; #pragma unroll
;         for (int a = 0; a < 2; ++a)
; #pragma unroll
;             for (int b = 0; b < 2; ++b)
; #pragma unroll
;                 for (int m = 0; m < 4; ++m)
; #pragma unroll
;                     for (int n = 0; n < 2; ++n) acc[a][b][m][n] = (f32x4){0.f, 0.f, 0.f, 0.f};
;         cur = nxt; cA = nA; cB = nB; ++ui;
;         if constexpr (GATHER) {
; #pragma unroll
;             for (int i = 0; i < 2; ++i) { voffA[i] = nvA0[i]; voffA1[i] = nvA1[i]; } }
;         if (wr == 1) PG8_BAR;
	v_pk_add_f32 v[24:25], v[72:73], v[12:13]
	v_pk_add_f32 v[26:27], v[46:47], v[2:3]
	v_pk_mul_f32 v[24:25], v[24:25], s[16:17] op_sel_hi:[1,0]
	v_pk_mul_f32 v[26:27], v[26:27], s[16:17] op_sel_hi:[1,0]
	v_cvt_pk_fp8_f32 v29, v24, v25 op_sel:[0,0,1]
	v_pk_add_f32 v[24:25], v[62:63], v[6:7]
	v_mov_b32_e32 v30, 0
	v_pk_mul_f32 v[24:25], v[24:25], s[16:17] op_sel_hi:[1,0]
	v_mov_b32_e32 v31, 0
	v_pk_add_f32 v[22:23], v[84:85], v[16:17]
	v_cvt_pk_fp8_f32 v30, v24, v25
	v_cvt_pk_fp8_f32 v31, v26, v27
	v_pk_mul_f32 v[22:23], v[22:23], s[16:17] op_sel_hi:[1,0]
	v_pk_add_f32 v[24:25], v[48:49], v[4:5]
	v_cvt_pk_fp8_f32 v28, v22, v23 op_sel:[0,0,1]
	v_pk_add_f32 v[22:23], v[64:65], v[8:9]
	v_pk_mul_f32 v[24:25], v[24:25], s[16:17] op_sel_hi:[1,0]
	v_pk_mul_f32 v[22:23], v[22:23], s[16:17] op_sel_hi:[1,0]
	v_cvt_pk_fp8_f32 v31, v24, v25 op_sel:[0,0,1]
	v_cvt_pk_fp8_f32 v30, v22, v23 op_sel:[0,0,1]
	v_add_co_u32_e32 v22, vcc, s91, v18
	v_pk_add_f32 v[26:27], v[42:43], v[10:11]
	s_nop 0
	v_addc_co_u32_e32 v23, vcc, 0, v19, vcc
	v_lshl_add_u64 v[20:21], v[18:19], 0, s[48:49]
	global_store_dwordx2 v[22:23], v[28:29], off
	global_store_dwordx2 v[20:21], v[30:31], off offset:128
	v_pk_mul_f32 v[26:27], v[26:27], s[16:17] op_sel_hi:[1,0]
	v_mov_b32_e32 v29, 0
	v_pk_add_f32 v[24:25], v[54:55], v[14:15]
	v_cvt_pk_fp8_f32 v29, v26, v27
	v_pk_mul_f32 v[24:25], v[24:25], s[16:17] op_sel_hi:[1,0]
	v_mov_b32_e32 v28, 0
	v_cvt_pk_fp8_f32 v28, v24, v25
	v_pk_add_f32 v[24:25], v[44:45], v[12:13]
	v_pk_add_f32 v[26:27], v[66:67], v[2:3]
	v_pk_mul_f32 v[24:25], v[24:25], s[16:17] op_sel_hi:[1,0]
	v_pk_mul_f32 v[26:27], v[26:27], s[16:17] op_sel_hi:[1,0]
	v_cvt_pk_fp8_f32 v29, v24, v25 op_sel:[0,0,1]
	v_pk_add_f32 v[24:25], v[74:75], v[6:7]
	v_mov_b32_e32 v30, 0
	v_pk_mul_f32 v[24:25], v[24:25], s[16:17] op_sel_hi:[1,0]
	v_mov_b32_e32 v31, 0
	v_pk_add_f32 v[22:23], v[56:57], v[16:17]
	v_cvt_pk_fp8_f32 v30, v24, v25
	v_cvt_pk_fp8_f32 v31, v26, v27
	v_pk_mul_f32 v[22:23], v[22:23], s[16:17] op_sel_hi:[1,0]
	v_pk_add_f32 v[24:25], v[68:69], v[4:5]
	v_cvt_pk_fp8_f32 v28, v22, v23 op_sel:[0,0,1]
	v_pk_add_f32 v[22:23], v[76:77], v[8:9]
	v_pk_mul_f32 v[24:25], v[24:25], s[16:17] op_sel_hi:[1,0]
	v_pk_mul_f32 v[22:23], v[22:23], s[16:17] op_sel_hi:[1,0]
	v_cvt_pk_fp8_f32 v31, v24, v25 op_sel:[0,0,1]
	v_cvt_pk_fp8_f32 v30, v22, v23 op_sel:[0,0,1]
	v_add_co_u32_e32 v22, vcc, s92, v18
	v_pk_add_f32 v[10:11], v[34:35], v[10:11]
	s_nop 0
	v_addc_co_u32_e32 v23, vcc, 0, v19, vcc
	v_lshl_add_u64 v[20:21], v[18:19], 0, s[50:51]
	global_store_dwordx2 v[22:23], v[28:29], off
	global_store_dwordx2 v[20:21], v[30:31], off offset:128
	v_pk_mul_f32 v[10:11], v[10:11], s[16:17] op_sel_hi:[1,0]
	v_mov_b32_e32 v23, 0
	v_cvt_pk_fp8_f32 v23, v10, v11
	v_pk_add_f32 v[14:15], v[38:39], v[14:15]
	v_pk_add_f32 v[10:11], v[36:37], v[12:13]
	v_pk_mul_f32 v[14:15], v[14:15], s[16:17] op_sel_hi:[1,0]
	v_mov_b32_e32 v22, 0
	v_pk_mul_f32 v[10:11], v[10:11], s[16:17] op_sel_hi:[1,0]
	v_pk_add_f32 v[6:7], v[58:59], v[6:7]
	v_pk_add_f32 v[2:3], v[50:51], v[2:3]
	v_cvt_pk_fp8_f32 v22, v14, v15
	v_cvt_pk_fp8_f32 v23, v10, v11 op_sel:[0,0,1]
	v_pk_mul_f32 v[6:7], v[6:7], s[16:17] op_sel_hi:[1,0]
	v_pk_mul_f32 v[2:3], v[2:3], s[16:17] op_sel_hi:[1,0]
	v_mov_b32_e32 v10, 0
	v_mov_b32_e32 v11, 0
	v_cvt_pk_fp8_f32 v10, v6, v7
	v_cvt_pk_fp8_f32 v11, v2, v3
	v_pk_add_f32 v[16:17], v[40:41], v[16:17]
	v_pk_add_f32 v[8:9], v[60:61], v[8:9]
	v_pk_mul_f32 v[16:17], v[16:17], s[16:17] op_sel_hi:[1,0]
	v_pk_add_f32 v[2:3], v[52:53], v[4:5]
	v_cvt_pk_fp8_f32 v22, v16, v17 op_sel:[0,0,1]
	v_pk_mul_f32 v[8:9], v[8:9], s[16:17] op_sel_hi:[1,0]
	v_pk_mul_f32 v[2:3], v[2:3], s[16:17] op_sel_hi:[1,0]
	v_cvt_pk_fp8_f32 v10, v8, v9 op_sel:[0,0,1]
	v_cvt_pk_fp8_f32 v11, v2, v3 op_sel:[0,0,1]
	v_add_co_u32_e32 v2, vcc, s93, v18
	v_lshl_add_u64 v[20:21], v[18:19], 0, s[52:53]
	s_nop 0
	v_addc_co_u32_e32 v3, vcc, 0, v19, vcc
	s_andn2_b64 vcc, exec, s[60:61]
	s_mov_b64 s[60:61], -1
	global_store_dwordx2 v[2:3], v[22:23], off
	global_store_dwordx2 v[20:21], v[10:11], off offset:128
	s_cbranch_vccnz .LBB0_2553
	s_andn2_b64 vcc, exec, s[8:9]
	s_cbranch_vccnz .LBB0_2552
	s_barrier
	s_branch .LBB0_2552
